# baseline (speedup 1.0000x reference)
.LBB13_5:
	v_lshlrev_b32_e32 v0, 2, v0
	v_and_b32_e32 v58, 0xfc, v0
	v_lshlrev_b64 v[4:5], 11, v[4:5]
	v_lshlrev_b32_e32 v0, 2, v58
	v_mov_b32_e32 v1, 0
	s_waitcnt lgkmcnt(0)
	v_lshl_add_u64 v[4:5], s[24:25], 0, v[4:5]
	v_lshl_add_u64 v[4:5], v[4:5], 0, v[0:1]
	global_load_dwordx4 v[8:11], v[4:5], off
	global_load_dwordx4 v[12:15], v0, s[20:21]
	global_load_dwordx4 v[16:19], v0, s[20:21] offset:1024
	global_load_dwordx4 v[20:23], v[4:5], off offset:1024
	v_lshlrev_b64 v[4:5], 11, v[2:3]
	v_lshl_add_u64 v[32:33], s[22:23], 0, v[4:5]
	v_lshl_add_u64 v[34:35], v[32:33], 0, v[0:1]
	v_lshl_add_u64 v[32:33], s[0:1], 2, v[32:33]
	global_load_dwordx4 v[24:27], v[34:35], off
	global_load_dwordx4 v[28:31], v[34:35], off offset:1024
	v_lshl_add_u64 v[40:41], v[32:33], 0, v[0:1]
	global_load_dwordx4 v[32:35], v[40:41], off
	global_load_dwordx4 v[36:39], v[40:41], off offset:1024
	global_load_dwordx4 v[44:47], v0, s[12:13] offset:1024
	v_lshlrev_b64 v[6:7], 11, v[6:7]
	global_load_dwordx4 v[40:43], v0, s[12:13]
	v_lshl_add_u64 v[6:7], s[18:19], 0, v[6:7]
	global_load_dwordx4 v[48:51], v0, s[14:15]
	v_lshl_add_u64 v[52:53], v[6:7], 0, v[0:1]
	v_mov_b32_e32 v59, 0x3727c5ac
	s_mov_b32 s12, 0xf800000
	v_mov_b32_e32 v60, 0x260
	v_lshl_add_u64 v[4:5], s[4:5], 0, v[4:5]
	v_lshlrev_b64 v[2:3], 10, v[2:3]
	s_waitcnt vmcnt(9)
	v_pk_add_f32 v[54:55], v[12:13], v[8:9]
	v_pk_add_f32 v[56:57], v[14:15], v[10:11]
	s_waitcnt vmcnt(7)
	v_pk_add_f32 v[20:21], v[16:17], v[20:21]
	v_pk_add_f32 v[18:19], v[18:19], v[22:23]
	global_load_dwordx4 v[6:9], v0, s[8:9]
	global_load_dwordx4 v[10:13], v0, s[10:11]
	global_load_dwordx4 v[14:17], v0, s[14:15] offset:1024
	s_waitcnt vmcnt(9)
	v_pk_add_f32 v[54:55], v[54:55], v[24:25]
	v_pk_add_f32 v[26:27], v[56:57], v[26:27]
	s_waitcnt vmcnt(8)
	v_pk_add_f32 v[28:29], v[20:21], v[28:29]
	v_pk_add_f32 v[30:31], v[18:19], v[30:31]
	global_load_dwordx4 v[18:21], v0, s[8:9] offset:1024
	global_load_dwordx4 v[22:25], v0, s[10:11] offset:1024
	s_waitcnt vmcnt(9)
	v_pk_add_f32 v[54:55], v[54:55], v[32:33]
	v_pk_add_f32 v[34:35], v[26:27], v[34:35]
	s_waitcnt vmcnt(8)
	v_pk_add_f32 v[36:37], v[28:29], v[36:37]
	v_pk_add_f32 v[38:39], v[30:31], v[38:39]
	global_load_dwordx4 v[26:29], v[52:53], off
	global_load_dwordx4 v[30:33], v[52:53], off offset:1024
	v_add_f32_e32 v52, 0, v54
	v_add_f32_e32 v52, v52, v55
	v_add_f32_e32 v52, v52, v34
	v_add_f32_e32 v52, v52, v35
	v_add_f32_e32 v52, v52, v36
	v_add_f32_e32 v52, v52, v37
	v_add_f32_e32 v52, v52, v38
	v_add_f32_e32 v52, v52, v39
	s_nop 1
	v_add_f32_dpp v52, v52, v52 quad_perm:[1,0,3,2] row_mask:0xf bank_mask:0xf bound_ctrl:1
	s_nop 1
	v_add_f32_dpp v52, v52, v52 quad_perm:[2,3,0,1] row_mask:0xf bank_mask:0xf bound_ctrl:1
	s_nop 1
	v_add_f32_dpp v52, v52, v52 row_half_mirror row_mask:0xf bank_mask:0xf bound_ctrl:1
	s_nop 1
	v_add_f32_dpp v52, v52, v52 row_mirror row_mask:0xf bank_mask:0xf bound_ctrl:1
	s_nop 0
	v_readlane_b32 s8, v52, 16
	v_readlane_b32 s9, v52, 48
	v_readlane_b32 s0, v52, 0
	v_readlane_b32 s1, v52, 32
	v_mov_b32_e32 v52, s8
	v_mov_b32_e32 v53, s9
	v_pk_add_f32 v[52:53], s[0:1], v[52:53]
	s_nop 0
	v_add_f32_e32 v52, v52, v53
	v_mul_f32_e32 v52, 0x3b000000, v52
	v_pk_add_f32 v[54:55], v[54:55], v[52:53] op_sel_hi:[1,0] neg_lo:[0,1] neg_hi:[0,1]
	v_pk_add_f32 v[34:35], v[34:35], v[52:53] op_sel_hi:[1,0] neg_lo:[0,1] neg_hi:[0,1]
	v_pk_add_f32 v[36:37], v[36:37], v[52:53] op_sel_hi:[1,0] neg_lo:[0,1] neg_hi:[0,1]
	v_pk_add_f32 v[38:39], v[38:39], v[52:53] op_sel_hi:[1,0] neg_lo:[0,1] neg_hi:[0,1]
	v_pk_mul_f32 v[52:53], v[54:55], v[54:55]
	s_waitcnt vmcnt(8)
	v_pk_mul_f32 v[40:41], v[40:41], v[54:55]
	v_add_f32_e32 v56, v52, v53
	v_pk_mul_f32 v[52:53], v[34:35], v[34:35]
	v_pk_mul_f32 v[34:35], v[42:43], v[34:35]
	v_add_f32_e32 v52, v56, v52
	v_add_f32_e32 v56, v52, v53
	v_pk_mul_f32 v[52:53], v[36:37], v[36:37]
	v_pk_mul_f32 v[36:37], v[44:45], v[36:37]
	v_add_f32_e32 v52, v56, v52
	v_add_f32_e32 v56, v52, v53
	v_pk_mul_f32 v[52:53], v[38:39], v[38:39]
	v_pk_mul_f32 v[38:39], v[46:47], v[38:39]
	v_add_f32_e32 v52, v56, v52
	v_add_f32_e32 v52, v52, v53
	s_nop 1
	v_add_f32_dpp v52, v52, v52 quad_perm:[1,0,3,2] row_mask:0xf bank_mask:0xf bound_ctrl:1
	s_nop 1
	v_add_f32_dpp v52, v52, v52 quad_perm:[2,3,0,1] row_mask:0xf bank_mask:0xf bound_ctrl:1
	s_nop 1
	v_add_f32_dpp v52, v52, v52 row_half_mirror row_mask:0xf bank_mask:0xf bound_ctrl:1
	s_nop 1
	v_add_f32_dpp v52, v52, v52 row_mirror row_mask:0xf bank_mask:0xf bound_ctrl:1
	s_nop 0
	v_readlane_b32 s8, v52, 16
	v_readlane_b32 s9, v52, 48
	v_readlane_b32 s0, v52, 0
	v_readlane_b32 s1, v52, 32
	v_mov_b32_e32 v52, s8
	v_mov_b32_e32 v53, s9
	v_pk_add_f32 v[52:53], s[0:1], v[52:53]
	s_nop 0
	v_add_f32_e32 v52, v52, v53
	v_fmamk_f32 v52, v52, 0x3b000000, v59
	v_mul_f32_e32 v53, 0x4f800000, v52
	v_cmp_gt_f32_e32 vcc, s12, v52
	s_nop 1
	v_cndmask_b32_e32 v52, v52, v53, vcc
	v_sqrt_f32_e32 v53, v52
	s_nop 0
	v_add_u32_e32 v42, -1, v53
	v_add_u32_e32 v43, 1, v53
	v_fma_f32 v44, -v42, v53, v52
	v_fma_f32 v45, -v43, v53, v52
	v_cmp_ge_f32_e64 s[0:1], 0, v44
	s_nop 1
	v_cndmask_b32_e64 v42, v53, v42, s[0:1]
	v_cmp_lt_f32_e64 s[0:1], 0, v45
	s_nop 1
	v_cndmask_b32_e64 v42, v42, v43, s[0:1]
	v_mul_f32_e32 v43, 0x37800000, v42
	v_cndmask_b32_e32 v42, v42, v43, vcc
	v_cmp_class_f32_e32 vcc, v52, v60
	s_nop 1
	v_cndmask_b32_e32 v42, v42, v52, vcc
	v_div_scale_f32 v43, s[0:1], v42, v42, 1.0
	v_rcp_f32_e32 v44, v43
	v_div_scale_f32 v45, vcc, 1.0, v42, 1.0
	v_fma_f32 v46, -v43, v44, 1.0
	v_fmac_f32_e32 v44, v46, v44
	v_mul_f32_e32 v46, v45, v44
	v_fma_f32 v47, -v43, v46, v45
	v_fmac_f32_e32 v46, v47, v44
	v_fma_f32 v43, -v43, v46, v45
	v_div_fmas_f32 v43, v43, v44, v46
	v_div_fixup_f32 v42, v43, v42, 1.0
	s_waitcnt vmcnt(7)
	v_pk_fma_f32 v[40:41], v[42:43], v[40:41], v[48:49] op_sel_hi:[0,1,1]
	s_waitcnt vmcnt(4)
	v_pk_fma_f32 v[14:15], v[42:43], v[36:37], v[14:15] op_sel_hi:[0,1,1]
	s_waitcnt vmcnt(1)
	v_pk_add_f32 v[26:27], v[40:41], v[26:27]
	v_pk_fma_f32 v[34:35], v[42:43], v[34:35], v[50:51] op_sel_hi:[0,1,1]
	s_waitcnt vmcnt(0)
	v_pk_add_f32 v[14:15], v[14:15], v[30:31]
	v_add_f32_e32 v30, 0, v26
	v_pk_add_f32 v[28:29], v[34:35], v[28:29]
	v_add_f32_e32 v30, v30, v27
	v_add_f32_e32 v30, v30, v28
	v_add_f32_e32 v30, v30, v29
	v_pk_fma_f32 v[16:17], v[42:43], v[38:39], v[16:17] op_sel_hi:[0,1,1]
	v_add_f32_e32 v30, v30, v14
	v_pk_add_f32 v[16:17], v[16:17], v[32:33]
	v_add_f32_e32 v30, v30, v15
	v_add_f32_e32 v30, v30, v16
	v_add_f32_e32 v30, v30, v17
	s_nop 1
	v_add_f32_dpp v30, v30, v30 quad_perm:[1,0,3,2] row_mask:0xf bank_mask:0xf bound_ctrl:1
	s_nop 1
	v_add_f32_dpp v30, v30, v30 quad_perm:[2,3,0,1] row_mask:0xf bank_mask:0xf bound_ctrl:1
	s_nop 1
	v_add_f32_dpp v30, v30, v30 row_half_mirror row_mask:0xf bank_mask:0xf bound_ctrl:1
	s_nop 1
	v_add_f32_dpp v30, v30, v30 row_mirror row_mask:0xf bank_mask:0xf bound_ctrl:1
	s_nop 0
	v_readlane_b32 s8, v30, 16
	v_readlane_b32 s9, v30, 48
	v_readlane_b32 s0, v30, 0
	v_readlane_b32 s1, v30, 32
	v_mov_b32_e32 v30, s8
	v_mov_b32_e32 v31, s9
	v_pk_add_f32 v[30:31], s[0:1], v[30:31]
	s_nop 0
	v_add_f32_e32 v30, v30, v31
	v_mul_f32_e32 v30, 0x3b000000, v30
	v_pk_add_f32 v[26:27], v[26:27], v[30:31] op_sel_hi:[1,0] neg_lo:[0,1] neg_hi:[0,1]
	v_pk_add_f32 v[28:29], v[28:29], v[30:31] op_sel_hi:[1,0] neg_lo:[0,1] neg_hi:[0,1]
	v_pk_add_f32 v[14:15], v[14:15], v[30:31] op_sel_hi:[1,0] neg_lo:[0,1] neg_hi:[0,1]
	v_pk_add_f32 v[16:17], v[16:17], v[30:31] op_sel_hi:[1,0] neg_lo:[0,1] neg_hi:[0,1]
	v_pk_mul_f32 v[30:31], v[26:27], v[26:27]
	v_pk_mul_f32 v[32:33], v[28:29], v[28:29]
	v_add_f32_e32 v30, v30, v31
	v_add_f32_e32 v30, v30, v32
	v_pk_mul_f32 v[34:35], v[14:15], v[14:15]
	v_add_f32_e32 v30, v30, v33
	v_add_f32_e32 v30, v30, v34
	v_pk_mul_f32 v[36:37], v[16:17], v[16:17]
	v_add_f32_e32 v30, v30, v35
	v_add_f32_e32 v30, v30, v36
	v_add_f32_e32 v30, v30, v37
	s_nop 1
	v_add_f32_dpp v30, v30, v30 quad_perm:[1,0,3,2] row_mask:0xf bank_mask:0xf bound_ctrl:1
	s_nop 1
	v_add_f32_dpp v30, v30, v30 quad_perm:[2,3,0,1] row_mask:0xf bank_mask:0xf bound_ctrl:1
	s_nop 1
	v_add_f32_dpp v30, v30, v30 row_half_mirror row_mask:0xf bank_mask:0xf bound_ctrl:1
	s_nop 1
	v_add_f32_dpp v30, v30, v30 row_mirror row_mask:0xf bank_mask:0xf bound_ctrl:1
	s_nop 0
	v_readlane_b32 s8, v30, 16
	v_readlane_b32 s9, v30, 48
	v_readlane_b32 s0, v30, 0
	v_readlane_b32 s1, v30, 32
	v_mov_b32_e32 v30, s8
	v_mov_b32_e32 v31, s9
	v_pk_add_f32 v[30:31], s[0:1], v[30:31]
	s_nop 0
	v_add_f32_e32 v30, v30, v31
	v_fmac_f32_e32 v59, 0x3b000000, v30
	v_mul_f32_e32 v30, 0x4f800000, v59
	v_cmp_gt_f32_e32 vcc, s12, v59
	s_nop 1
	v_cndmask_b32_e32 v30, v59, v30, vcc
	v_sqrt_f32_e32 v31, v30
	s_nop 0
	v_add_u32_e32 v32, -1, v31
	v_fma_f32 v33, -v32, v31, v30
	v_cmp_ge_f32_e64 s[0:1], 0, v33
	v_add_u32_e32 v33, 1, v31
	s_nop 0
	v_cndmask_b32_e64 v32, v31, v32, s[0:1]
	v_fma_f32 v31, -v33, v31, v30
	v_cmp_lt_f32_e64 s[0:1], 0, v31
	s_nop 1
	v_cndmask_b32_e64 v31, v32, v33, s[0:1]
	v_mul_f32_e32 v32, 0x37800000, v31
	v_cndmask_b32_e32 v31, v31, v32, vcc
	v_cmp_class_f32_e32 vcc, v30, v60
	s_nop 1
	v_cndmask_b32_e32 v32, v31, v30, vcc
	v_div_scale_f32 v33, s[0:1], v32, v32, 1.0
	v_rcp_f32_e32 v34, v33
	v_lshl_add_u64 v[30:31], v[4:5], 0, v[0:1]
	s_mov_b32 s0, 0x43000000
	v_fma_f32 v0, -v33, v34, 1.0
	v_fmac_f32_e32 v34, v0, v34
	v_div_scale_f32 v0, vcc, 1.0, v32, 1.0
	v_mul_f32_e32 v4, v0, v34
	v_fma_f32 v5, -v33, v4, v0
	v_fmac_f32_e32 v4, v5, v34
	v_fma_f32 v0, -v33, v4, v0
	v_div_fmas_f32 v0, v0, v34, v4
	v_div_fixup_f32 v0, v0, v32, 1.0
	v_pk_mul_f32 v[4:5], v[6:7], v[26:27]
	v_pk_mul_f32 v[6:7], v[8:9], v[28:29]
	v_pk_fma_f32 v[4:5], v[0:1], v[4:5], v[10:11] op_sel_hi:[0,1,1]
	v_pk_mul_f32 v[8:9], v[18:19], v[14:15]
	v_pk_fma_f32 v[6:7], v[0:1], v[6:7], v[12:13] op_sel_hi:[0,1,1]
	v_pk_fma_f32 v[8:9], v[0:1], v[8:9], v[22:23] op_sel_hi:[0,1,1]
	v_pk_mul_f32 v[10:11], v[20:21], v[16:17]
	v_fma_mixlo_f16 v12, v4, s0, 0
	v_pk_fma_f32 v[10:11], v[0:1], v[10:11], v[24:25] op_sel_hi:[0,1,1]
	global_store_dwordx4 v[30:31], v[4:7], off sc1
	global_store_dwordx4 v[30:31], v[8:11], off offset:1024 sc1
	v_mul_f32_e32 v0, 0x43000000, v4
	v_fma_mixlo_f16 v4, v4, s0, -v12 op_sel_hi:[0,0,1]
	v_fma_mixlo_f16 v12, v8, s0, 0
	v_mul_f32_e32 v13, 0x43000000, v8
	v_fma_mixlo_f16 v8, v8, s0, -v12 op_sel_hi:[0,0,1]
	v_mul_f32_e32 v12, 0x43000000, v5
	v_fma_mixlo_f16 v14, v5, s0, 0
	v_cvt_pk_f16_f32 v12, v0, v12
	v_mul_f32_e32 v0, 0x43000000, v9
	v_pk_mul_f32 v[16:17], v[6:7], s[0:1] op_sel_hi:[1,0]
	v_fma_mixhi_f16 v4, v5, s0, -v14 op_sel_hi:[0,0,1]
	v_cvt_pk_f16_f32 v14, v13, v0
	v_cvt_pk_f16_f32 v13, v16, v17
	v_pk_mul_f32 v[18:19], v[10:11], s[0:1] op_sel_hi:[1,0]
	v_cvt_f32_f16_e32 v16, v13
	v_cvt_f32_f16_sdwa v17, v13 dst_sel:DWORD dst_unused:UNUSED_PAD src0_sel:WORD_1
	v_cvt_pk_f16_f32 v15, v18, v19
	v_cvt_f32_f16_e32 v18, v15
	v_cvt_f32_f16_sdwa v19, v15 dst_sel:DWORD dst_unused:UNUSED_PAD src0_sel:WORD_1
	v_fma_mixlo_f16 v5, v9, s0, 0
	v_pk_fma_f32 v[6:7], v[6:7], s[0:1], v[16:17] op_sel_hi:[1,0,1] neg_lo:[0,0,1] neg_hi:[0,0,1]
	v_fma_mixhi_f16 v8, v9, s0, -v5 op_sel_hi:[0,0,1]
	v_cvt_pk_f16_f32 v5, v6, v7
	v_pk_fma_f32 v[6:7], v[10:11], s[0:1], v[18:19] op_sel_hi:[1,0,1] neg_lo:[0,0,1] neg_hi:[0,0,1]
	v_lshlrev_b32_e32 v0, 1, v58
	v_cvt_pk_f16_f32 v9, v6, v7
	v_lshl_add_u64 v[6:7], s[6:7], 0, v[2:3]
	v_lshl_add_u64 v[2:3], s[2:3], 0, v[2:3]
	v_lshl_add_u64 v[6:7], v[6:7], 0, v[0:1]
	v_lshl_add_u64 v[0:1], v[2:3], 0, v[0:1]
	v_mbcnt_lo_u32_b32 v20, -1, 0
	v_mbcnt_hi_u32_b32 v20, -1, v20
	v_and_b32_e32 v20, 1, v20
	v_cmp_eq_u32_e32 vcc, 1, v20
	v_mul_u32_u24_e32 v22, 0x1f8, v20
	v_mov_b32_e32 v23, 0
	s_nop 1
	v_mov_b32_dpp v24, v12 quad_perm:[1,0,3,2] row_mask:0xf bank_mask:0xf
	v_mov_b32_dpp v25, v13 quad_perm:[1,0,3,2] row_mask:0xf bank_mask:0xf
	v_mov_b32_dpp v26, v14 quad_perm:[1,0,3,2] row_mask:0xf bank_mask:0xf
	v_mov_b32_dpp v27, v15 quad_perm:[1,0,3,2] row_mask:0xf bank_mask:0xf
	s_nop 1
	v_cndmask_b32_e32 v28, v12, v26, vcc
	v_cndmask_b32_e32 v29, v13, v27, vcc
	v_cndmask_b32_e32 v30, v24, v14, vcc
	v_cndmask_b32_e32 v31, v25, v15, vcc
	v_lshl_add_u64 v[32:33], v[6:7], 0, v[22:23]
	global_store_dwordx4 v[32:33], v[28:31], off sc1
	s_nop 1
	v_mov_b32_dpp v24, v4 quad_perm:[1,0,3,2] row_mask:0xf bank_mask:0xf
	v_mov_b32_dpp v25, v5 quad_perm:[1,0,3,2] row_mask:0xf bank_mask:0xf
	v_mov_b32_dpp v26, v8 quad_perm:[1,0,3,2] row_mask:0xf bank_mask:0xf
	v_mov_b32_dpp v27, v9 quad_perm:[1,0,3,2] row_mask:0xf bank_mask:0xf
	s_nop 1
	v_cndmask_b32_e32 v28, v4, v26, vcc
	v_cndmask_b32_e32 v29, v5, v27, vcc
	v_cndmask_b32_e32 v30, v24, v8, vcc
	v_cndmask_b32_e32 v31, v25, v9, vcc
	v_lshl_add_u64 v[32:33], v[0:1], 0, v[22:23]
	global_store_dwordx4 v[32:33], v[28:31], off sc1
	s_nop 1
	s_endpgm
	s_endpgm
	s_endpgm
	s_endpgm
	s_endpgm
	s_endpgm
	s_endpgm
	s_endpgm
	s_endpgm
	s_endpgm
	s_endpgm
	s_endpgm
	s_endpgm
	s_endpgm
	s_endpgm
	s_endpgm
	s_endpgm
	s_endpgm
	s_endpgm
	s_endpgm
	s_endpgm
	s_endpgm
	s_endpgm
	s_endpgm
	s_endpgm
	s_endpgm
	s_endpgm
	s_endpgm
	s_endpgm
	s_endpgm
	s_endpgm
	s_endpgm
	s_endpgm
	s_endpgm
	s_endpgm
	s_endpgm
	s_endpgm
	s_endpgm
	s_endpgm
	s_endpgm
	s_endpgm
	s_endpgm
	s_endpgm
	s_endpgm
	s_endpgm
	s_endpgm
	s_endpgm
	s_endpgm
	s_endpgm
	s_endpgm
	s_endpgm
	s_endpgm
	s_endpgm

.LBB14_5:
	v_lshlrev_b32_e32 v0, 2, v0
	v_and_b32_e32 v60, 0xfc, v0
	v_lshlrev_b64 v[8:9], 11, v[8:9]
	v_lshlrev_b32_e32 v0, 2, v60
	v_mov_b32_e32 v1, 0
	s_waitcnt lgkmcnt(0)
	v_lshl_add_u64 v[8:9], s[24:25], 0, v[8:9]
	v_lshl_add_u64 v[24:25], v[8:9], 0, v[0:1]
	global_load_dwordx4 v[8:11], v[24:25], off
	global_load_dwordx4 v[12:15], v0, s[20:21]
	global_load_dwordx4 v[16:19], v0, s[20:21] offset:1024
	global_load_dwordx4 v[20:23], v[24:25], off offset:1024
	v_lshlrev_b64 v[4:5], 11, v[2:3]
	v_lshl_add_u64 v[36:37], s[22:23], 0, v[4:5]
	v_lshl_add_u64 v[28:29], v[36:37], 0, v[0:1]
	global_load_dwordx4 v[24:27], v[28:29], off
	s_waitcnt lgkmcnt(0)
	v_lshl_add_u64 v[30:31], s[0:1], 2, v[36:37]
	v_lshl_add_u64 v[38:39], v[30:31], 0, v[0:1]
	v_lshl_add_u64 v[32:33], s[0:1], 3, v[36:37]
	v_lshl_add_u64 v[44:45], v[32:33], 0, v[0:1]
	global_load_dwordx4 v[32:35], v[38:39], off
	v_mad_u64_u32 v[48:49], s[16:17], s0, 12, v[36:37]
	global_load_dwordx4 v[28:31], v[28:29], off offset:1024
	v_mov_b32_e32 v40, v49
	v_mad_u64_u32 v[46:47], s[0:1], s1, 12, v[40:41]
	global_load_dwordx4 v[40:43], v[44:45], off
	v_mov_b32_e32 v49, v46
	v_lshl_add_u64 v[56:57], v[48:49], 0, v[0:1]
	global_load_dwordx4 v[36:39], v[38:39], off offset:1024
	v_lshlrev_b64 v[6:7], 11, v[6:7]
	global_load_dwordx4 v[44:47], v[44:45], off offset:1024
	s_nop 0
	global_load_dwordx4 v[48:51], v[56:57], off
	global_load_dwordx4 v[52:55], v[56:57], off offset:1024
	v_lshl_add_u64 v[6:7], s[18:19], 0, v[6:7]
	v_lshl_add_u64 v[56:57], v[6:7], 0, v[0:1]
	v_mov_b32_e32 v61, 0x3727c5ac
	s_mov_b32 s16, 0xf800000
	v_lshl_add_u64 v[4:5], s[4:5], 0, v[4:5]
	v_lshlrev_b64 v[2:3], 10, v[2:3]
	s_waitcnt vmcnt(10)
	v_pk_add_f32 v[58:59], v[12:13], v[8:9]
	v_pk_add_f32 v[14:15], v[14:15], v[10:11]
	global_load_dwordx4 v[6:9], v0, s[12:13]
	global_load_dwordx4 v[10:13], v0, s[14:15]
	s_waitcnt vmcnt(10)
	v_pk_add_f32 v[16:17], v[16:17], v[20:21]
	v_pk_add_f32 v[18:19], v[18:19], v[22:23]
	s_waitcnt vmcnt(9)
	v_pk_add_f32 v[22:23], v[58:59], v[24:25]
	v_pk_add_f32 v[24:25], v[14:15], v[26:27]
	s_waitcnt vmcnt(8)
	v_pk_add_f32 v[32:33], v[22:23], v[32:33]
	v_pk_add_f32 v[34:35], v[24:25], v[34:35]
	s_waitcnt vmcnt(7)
	v_pk_add_f32 v[58:59], v[16:17], v[28:29]
	v_pk_add_f32 v[30:31], v[18:19], v[30:31]
	global_load_dwordx4 v[14:17], v0, s[12:13] offset:1024
	global_load_dwordx4 v[18:21], v0, s[14:15] offset:1024
	global_load_dwordx4 v[22:25], v[56:57], off
	global_load_dwordx4 v[26:29], v[56:57], off offset:1024
	s_waitcnt vmcnt(10)
	v_pk_add_f32 v[32:33], v[32:33], v[40:41]
	v_pk_add_f32 v[34:35], v[34:35], v[42:43]
	s_waitcnt vmcnt(9)
	v_pk_add_f32 v[30:31], v[30:31], v[38:39]
	v_pk_add_f32 v[36:37], v[58:59], v[36:37]
	s_waitcnt vmcnt(7)
	v_pk_add_f32 v[32:33], v[32:33], v[48:49]
	v_pk_add_f32 v[34:35], v[34:35], v[50:51]
	v_add_f32_e32 v38, 0, v32
	v_add_f32_e32 v38, v38, v33
	v_pk_add_f32 v[36:37], v[36:37], v[44:45]
	v_add_f32_e32 v38, v38, v34
	s_waitcnt vmcnt(6)
	v_pk_add_f32 v[36:37], v[36:37], v[52:53]
	v_add_f32_e32 v38, v38, v35
	v_pk_add_f32 v[30:31], v[30:31], v[46:47]
	v_add_f32_e32 v38, v38, v36
	v_pk_add_f32 v[30:31], v[30:31], v[54:55]
	v_add_f32_e32 v38, v38, v37
	v_add_f32_e32 v38, v38, v30
	v_add_f32_e32 v38, v38, v31
	v_mov_b32_e32 v55, 0x260
	s_nop 0
	v_add_f32_dpp v38, v38, v38 quad_perm:[1,0,3,2] row_mask:0xf bank_mask:0xf bound_ctrl:1
	s_nop 1
	v_add_f32_dpp v38, v38, v38 quad_perm:[2,3,0,1] row_mask:0xf bank_mask:0xf bound_ctrl:1
	s_nop 1
	v_add_f32_dpp v38, v38, v38 row_half_mirror row_mask:0xf bank_mask:0xf bound_ctrl:1
	s_nop 1
	v_add_f32_dpp v38, v38, v38 row_mirror row_mask:0xf bank_mask:0xf bound_ctrl:1
	s_nop 0
	v_readlane_b32 s12, v38, 16
	v_readlane_b32 s13, v38, 48
	v_readlane_b32 s0, v38, 0
	v_readlane_b32 s1, v38, 32
	v_mov_b32_e32 v38, s12
	v_mov_b32_e32 v39, s13
	v_pk_add_f32 v[38:39], s[0:1], v[38:39]
	s_nop 0
	v_add_f32_e32 v38, v38, v39
	v_mul_f32_e32 v38, 0x3b000000, v38
	v_pk_add_f32 v[46:47], v[32:33], v[38:39] op_sel_hi:[1,0] neg_lo:[0,1] neg_hi:[0,1]
	v_pk_add_f32 v[48:49], v[34:35], v[38:39] op_sel_hi:[1,0] neg_lo:[0,1] neg_hi:[0,1]
	v_pk_add_f32 v[52:53], v[30:31], v[38:39] op_sel_hi:[1,0] neg_lo:[0,1] neg_hi:[0,1]
	v_pk_mul_f32 v[30:31], v[46:47], v[46:47]
	v_pk_mul_f32 v[32:33], v[48:49], v[48:49]
	v_add_f32_e32 v30, v30, v31
	v_pk_add_f32 v[50:51], v[36:37], v[38:39] op_sel_hi:[1,0] neg_lo:[0,1] neg_hi:[0,1]
	v_add_f32_e32 v30, v30, v32
	v_pk_mul_f32 v[34:35], v[50:51], v[50:51]
	v_add_f32_e32 v30, v30, v33
	v_add_f32_e32 v30, v30, v34
	v_pk_mul_f32 v[36:37], v[52:53], v[52:53]
	v_add_f32_e32 v30, v30, v35
	v_add_f32_e32 v30, v30, v36
	v_add_f32_e32 v30, v30, v37
	s_waitcnt vmcnt(5)
	v_pk_mul_f32 v[6:7], v[6:7], v[46:47]
	v_add_f32_dpp v30, v30, v30 quad_perm:[1,0,3,2] row_mask:0xf bank_mask:0xf bound_ctrl:1
	v_pk_mul_f32 v[8:9], v[8:9], v[48:49]
	s_nop 0
	v_add_f32_dpp v30, v30, v30 quad_perm:[2,3,0,1] row_mask:0xf bank_mask:0xf bound_ctrl:1
	s_nop 1
	v_add_f32_dpp v30, v30, v30 row_half_mirror row_mask:0xf bank_mask:0xf bound_ctrl:1
	s_nop 1
	v_add_f32_dpp v30, v30, v30 row_mirror row_mask:0xf bank_mask:0xf bound_ctrl:1
	s_nop 0
	v_readlane_b32 s12, v30, 16
	v_readlane_b32 s13, v30, 48
	v_readlane_b32 s0, v30, 0
	v_readlane_b32 s1, v30, 32
	v_mov_b32_e32 v30, s12
	v_mov_b32_e32 v31, s13
	v_pk_add_f32 v[30:31], s[0:1], v[30:31]
	s_nop 0
	v_add_f32_e32 v30, v30, v31
	v_fmamk_f32 v30, v30, 0x3b000000, v61
	v_mul_f32_e32 v31, 0x4f800000, v30
	v_cmp_gt_f32_e32 vcc, s16, v30
	s_nop 1
	v_cndmask_b32_e32 v54, v30, v31, vcc
	v_sqrt_f32_e32 v38, v54
	global_load_dwordx4 v[30:33], v0, s[8:9]
	global_load_dwordx4 v[34:37], v0, s[10:11]
	v_add_u32_e32 v39, -1, v38
	v_add_u32_e32 v56, 1, v38
	v_fma_f32 v40, -v39, v38, v54
	v_fma_f32 v41, -v56, v38, v54
	v_cmp_ge_f32_e64 s[0:1], 0, v40
	s_nop 1
	v_cndmask_b32_e64 v57, v38, v39, s[0:1]
	v_cmp_lt_f32_e64 s[0:1], 0, v41
	global_load_dwordx4 v[38:41], v0, s[8:9] offset:1024
	global_load_dwordx4 v[42:45], v0, s[10:11] offset:1024
	v_cndmask_b32_e64 v46, v57, v56, s[0:1]
	v_mul_f32_e32 v47, 0x37800000, v46
	v_cndmask_b32_e32 v46, v46, v47, vcc
	v_cmp_class_f32_e32 vcc, v54, v55
	s_nop 1
	v_cndmask_b32_e32 v46, v46, v54, vcc
	v_div_scale_f32 v47, s[0:1], v46, v46, 1.0
	v_rcp_f32_e32 v54, v47
	v_div_scale_f32 v48, vcc, 1.0, v46, 1.0
	v_fma_f32 v49, -v47, v54, 1.0
	v_fmac_f32_e32 v54, v49, v54
	v_mul_f32_e32 v49, v48, v54
	v_fma_f32 v56, -v47, v49, v48
	v_fmac_f32_e32 v49, v56, v54
	v_fma_f32 v47, -v47, v49, v48
	v_div_fmas_f32 v47, v47, v54, v49
	v_div_fixup_f32 v46, v47, v46, 1.0
	s_waitcnt vmcnt(8)
	v_pk_fma_f32 v[6:7], v[46:47], v[6:7], v[10:11] op_sel_hi:[0,1,1]
	s_waitcnt vmcnt(5)
	v_pk_add_f32 v[6:7], v[6:7], v[22:23]
	v_pk_fma_f32 v[8:9], v[46:47], v[8:9], v[12:13] op_sel_hi:[0,1,1]
	v_pk_mul_f32 v[10:11], v[14:15], v[50:51]
	v_add_f32_e32 v14, 0, v6
	v_add_f32_e32 v14, v14, v7
	v_pk_add_f32 v[8:9], v[8:9], v[24:25]
	v_pk_fma_f32 v[10:11], v[46:47], v[10:11], v[18:19] op_sel_hi:[0,1,1]
	v_add_f32_e32 v14, v14, v8
	v_pk_mul_f32 v[12:13], v[16:17], v[52:53]
	v_add_f32_e32 v14, v14, v9
	s_waitcnt vmcnt(4)
	v_pk_add_f32 v[10:11], v[10:11], v[26:27]
	v_pk_fma_f32 v[12:13], v[46:47], v[12:13], v[20:21] op_sel_hi:[0,1,1]
	v_add_f32_e32 v14, v14, v10
	v_add_f32_e32 v14, v14, v11
	v_pk_add_f32 v[12:13], v[12:13], v[28:29]
	s_nop 0
	v_add_f32_e32 v14, v14, v12
	v_add_f32_e32 v14, v14, v13
	s_nop 1
	v_add_f32_dpp v14, v14, v14 quad_perm:[1,0,3,2] row_mask:0xf bank_mask:0xf bound_ctrl:1
	s_nop 1
	v_add_f32_dpp v14, v14, v14 quad_perm:[2,3,0,1] row_mask:0xf bank_mask:0xf bound_ctrl:1
	s_nop 1
	v_add_f32_dpp v14, v14, v14 row_half_mirror row_mask:0xf bank_mask:0xf bound_ctrl:1
	s_nop 1
	v_add_f32_dpp v14, v14, v14 row_mirror row_mask:0xf bank_mask:0xf bound_ctrl:1
	s_nop 0
	v_readlane_b32 s8, v14, 16
	v_readlane_b32 s9, v14, 48
	v_readlane_b32 s0, v14, 0
	v_readlane_b32 s1, v14, 32
	v_mov_b32_e32 v14, s8
	v_mov_b32_e32 v15, s9
	v_pk_add_f32 v[14:15], s[0:1], v[14:15]
	s_nop 0
	v_add_f32_e32 v14, v14, v15
	v_mul_f32_e32 v14, 0x3b000000, v14
	v_pk_add_f32 v[6:7], v[6:7], v[14:15] op_sel_hi:[1,0] neg_lo:[0,1] neg_hi:[0,1]
	v_pk_add_f32 v[8:9], v[8:9], v[14:15] op_sel_hi:[1,0] neg_lo:[0,1] neg_hi:[0,1]
	v_pk_mul_f32 v[16:17], v[6:7], v[6:7]
	v_pk_mul_f32 v[18:19], v[8:9], v[8:9]
	v_add_f32_e32 v16, v16, v17
	v_pk_add_f32 v[10:11], v[10:11], v[14:15] op_sel_hi:[1,0] neg_lo:[0,1] neg_hi:[0,1]
	v_add_f32_e32 v16, v16, v18
	v_pk_mul_f32 v[20:21], v[10:11], v[10:11]
	v_add_f32_e32 v16, v16, v19
	v_pk_add_f32 v[12:13], v[12:13], v[14:15] op_sel_hi:[1,0] neg_lo:[0,1] neg_hi:[0,1]
	v_add_f32_e32 v16, v16, v20
	v_pk_mul_f32 v[14:15], v[12:13], v[12:13]
	v_add_f32_e32 v16, v16, v21
	v_add_f32_e32 v14, v16, v14
	v_add_f32_e32 v14, v14, v15
	s_nop 1
	v_add_f32_dpp v14, v14, v14 quad_perm:[1,0,3,2] row_mask:0xf bank_mask:0xf bound_ctrl:1
	s_nop 1
	v_add_f32_dpp v14, v14, v14 quad_perm:[2,3,0,1] row_mask:0xf bank_mask:0xf bound_ctrl:1
	s_nop 1
	v_add_f32_dpp v14, v14, v14 row_half_mirror row_mask:0xf bank_mask:0xf bound_ctrl:1
	s_nop 1
	v_add_f32_dpp v14, v14, v14 row_mirror row_mask:0xf bank_mask:0xf bound_ctrl:1
	s_nop 0
	v_readlane_b32 s8, v14, 16
	v_readlane_b32 s9, v14, 48
	v_readlane_b32 s0, v14, 0
	v_readlane_b32 s1, v14, 32
	v_mov_b32_e32 v14, s8
	v_mov_b32_e32 v15, s9
	v_pk_add_f32 v[14:15], s[0:1], v[14:15]
	s_nop 0
	v_add_f32_e32 v14, v14, v15
	v_fmac_f32_e32 v61, 0x3b000000, v14
	v_mul_f32_e32 v14, 0x4f800000, v61
	v_cmp_gt_f32_e32 vcc, s16, v61
	s_nop 1
	v_cndmask_b32_e32 v14, v61, v14, vcc
	v_sqrt_f32_e32 v15, v14
	s_nop 0
	v_add_u32_e32 v16, -1, v15
	v_fma_f32 v17, -v16, v15, v14
	v_cmp_ge_f32_e64 s[0:1], 0, v17
	v_add_u32_e32 v17, 1, v15
	s_nop 0
	v_cndmask_b32_e64 v16, v15, v16, s[0:1]
	v_fma_f32 v15, -v17, v15, v14
	v_cmp_lt_f32_e64 s[0:1], 0, v15
	s_nop 1
	v_cndmask_b32_e64 v15, v16, v17, s[0:1]
	v_mul_f32_e32 v16, 0x37800000, v15
	v_cndmask_b32_e32 v15, v15, v16, vcc
	v_cmp_class_f32_e32 vcc, v14, v55
	s_nop 1
	v_cndmask_b32_e32 v16, v15, v14, vcc
	v_div_scale_f32 v17, s[0:1], v16, v16, 1.0
	v_rcp_f32_e32 v18, v17
	v_lshl_add_u64 v[14:15], v[4:5], 0, v[0:1]
	s_mov_b32 s0, 0x43000000
	v_fma_f32 v0, -v17, v18, 1.0
	v_fmac_f32_e32 v18, v0, v18
	v_div_scale_f32 v0, vcc, 1.0, v16, 1.0
	v_mul_f32_e32 v4, v0, v18
	v_fma_f32 v5, -v17, v4, v0
	v_fmac_f32_e32 v4, v5, v18
	v_fma_f32 v0, -v17, v4, v0
	v_div_fmas_f32 v0, v0, v18, v4
	v_div_fixup_f32 v0, v0, v16, 1.0
	s_waitcnt vmcnt(3)
	v_pk_mul_f32 v[4:5], v[30:31], v[6:7]
	v_pk_mul_f32 v[6:7], v[32:33], v[8:9]
	s_waitcnt vmcnt(2)
	v_pk_fma_f32 v[4:5], v[0:1], v[4:5], v[34:35] op_sel_hi:[0,1,1]
	s_waitcnt vmcnt(1)
	v_pk_mul_f32 v[8:9], v[38:39], v[10:11]
	v_pk_fma_f32 v[6:7], v[0:1], v[6:7], v[36:37] op_sel_hi:[0,1,1]
	s_waitcnt vmcnt(0)
	v_pk_fma_f32 v[8:9], v[0:1], v[8:9], v[42:43] op_sel_hi:[0,1,1]
	v_pk_mul_f32 v[10:11], v[40:41], v[12:13]
	v_fma_mixlo_f16 v12, v4, s0, 0
	v_pk_fma_f32 v[10:11], v[0:1], v[10:11], v[44:45] op_sel_hi:[0,1,1]
	global_store_dwordx4 v[14:15], v[4:7], off sc1
	global_store_dwordx4 v[14:15], v[8:11], off offset:1024 sc1
	v_mul_f32_e32 v0, 0x43000000, v4
	v_fma_mixlo_f16 v4, v4, s0, -v12 op_sel_hi:[0,0,1]
	v_fma_mixlo_f16 v12, v8, s0, 0
	v_mul_f32_e32 v13, 0x43000000, v8
	v_fma_mixlo_f16 v8, v8, s0, -v12 op_sel_hi:[0,0,1]
	v_mul_f32_e32 v12, 0x43000000, v5
	v_fma_mixlo_f16 v14, v5, s0, 0
	v_cvt_pk_f16_f32 v12, v0, v12
	v_mul_f32_e32 v0, 0x43000000, v9
	v_pk_mul_f32 v[16:17], v[6:7], s[0:1] op_sel_hi:[1,0]
	v_fma_mixhi_f16 v4, v5, s0, -v14 op_sel_hi:[0,0,1]
	v_cvt_pk_f16_f32 v14, v13, v0
	v_cvt_pk_f16_f32 v13, v16, v17
	v_pk_mul_f32 v[18:19], v[10:11], s[0:1] op_sel_hi:[1,0]
	v_cvt_f32_f16_e32 v16, v13
	v_cvt_f32_f16_sdwa v17, v13 dst_sel:DWORD dst_unused:UNUSED_PAD src0_sel:WORD_1
	v_cvt_pk_f16_f32 v15, v18, v19
	v_cvt_f32_f16_e32 v18, v15
	v_cvt_f32_f16_sdwa v19, v15 dst_sel:DWORD dst_unused:UNUSED_PAD src0_sel:WORD_1
	v_fma_mixlo_f16 v5, v9, s0, 0
	v_pk_fma_f32 v[6:7], v[6:7], s[0:1], v[16:17] op_sel_hi:[1,0,1] neg_lo:[0,0,1] neg_hi:[0,0,1]
	v_fma_mixhi_f16 v8, v9, s0, -v5 op_sel_hi:[0,0,1]
	v_cvt_pk_f16_f32 v5, v6, v7
	v_pk_fma_f32 v[6:7], v[10:11], s[0:1], v[18:19] op_sel_hi:[1,0,1] neg_lo:[0,0,1] neg_hi:[0,0,1]
	v_lshlrev_b32_e32 v0, 1, v60
	v_cvt_pk_f16_f32 v9, v6, v7
	v_lshl_add_u64 v[6:7], s[6:7], 0, v[2:3]
	v_lshl_add_u64 v[2:3], s[2:3], 0, v[2:3]
	v_lshl_add_u64 v[6:7], v[6:7], 0, v[0:1]
	v_lshl_add_u64 v[0:1], v[2:3], 0, v[0:1]
	v_mbcnt_lo_u32_b32 v20, -1, 0
	v_mbcnt_hi_u32_b32 v20, -1, v20
	v_and_b32_e32 v20, 1, v20
	v_cmp_eq_u32_e32 vcc, 1, v20
	v_mul_u32_u24_e32 v22, 0x1f8, v20
	v_mov_b32_e32 v23, 0
	s_nop 1
	v_mov_b32_dpp v24, v12 quad_perm:[1,0,3,2] row_mask:0xf bank_mask:0xf
	v_mov_b32_dpp v25, v13 quad_perm:[1,0,3,2] row_mask:0xf bank_mask:0xf
	v_mov_b32_dpp v26, v14 quad_perm:[1,0,3,2] row_mask:0xf bank_mask:0xf
	v_mov_b32_dpp v27, v15 quad_perm:[1,0,3,2] row_mask:0xf bank_mask:0xf
	s_nop 1
	v_cndmask_b32_e32 v28, v12, v26, vcc
	v_cndmask_b32_e32 v29, v13, v27, vcc
	v_cndmask_b32_e32 v30, v24, v14, vcc
	v_cndmask_b32_e32 v31, v25, v15, vcc
	v_lshl_add_u64 v[32:33], v[6:7], 0, v[22:23]
	global_store_dwordx4 v[32:33], v[28:31], off sc1
	s_nop 1
	v_mov_b32_dpp v24, v4 quad_perm:[1,0,3,2] row_mask:0xf bank_mask:0xf
	v_mov_b32_dpp v25, v5 quad_perm:[1,0,3,2] row_mask:0xf bank_mask:0xf
	v_mov_b32_dpp v26, v8 quad_perm:[1,0,3,2] row_mask:0xf bank_mask:0xf
	v_mov_b32_dpp v27, v9 quad_perm:[1,0,3,2] row_mask:0xf bank_mask:0xf
	s_nop 1
	v_cndmask_b32_e32 v28, v4, v26, vcc
	v_cndmask_b32_e32 v29, v5, v27, vcc
	v_cndmask_b32_e32 v30, v24, v8, vcc
	v_cndmask_b32_e32 v31, v25, v9, vcc
	v_lshl_add_u64 v[32:33], v[0:1], 0, v[22:23]
	global_store_dwordx4 v[32:33], v[28:31], off sc1
	s_nop 1
	s_endpgm
	s_endpgm
	s_endpgm
	s_endpgm
	s_endpgm
	s_endpgm
	s_endpgm
	s_endpgm
	s_endpgm
	s_endpgm
	s_endpgm

.LBB15_5:
	v_lshlrev_b32_e32 v0, 2, v0
	v_and_b32_e32 v8, 0xfc, v0
	v_lshlrev_b64 v[4:5], 11, v[4:5]
	v_lshlrev_b32_e32 v0, 2, v8
	v_mov_b32_e32 v1, 0
	s_waitcnt lgkmcnt(0)
	v_lshl_add_u64 v[4:5], s[24:25], 0, v[4:5]
	v_lshl_add_u64 v[4:5], v[4:5], 0, v[0:1]
	global_load_dwordx4 v[10:13], v[4:5], off
	global_load_dwordx4 v[14:17], v0, s[20:21]
	global_load_dwordx4 v[18:21], v0, s[20:21] offset:1024
	global_load_dwordx4 v[22:25], v[4:5], off offset:1024
	v_lshlrev_b64 v[4:5], 11, v[2:3]
	v_lshl_add_u64 v[50:51], s[22:23], 0, v[4:5]
	v_lshl_add_u64 v[30:31], v[50:51], 0, v[0:1]
	global_load_dwordx4 v[26:29], v[30:31], off
	s_waitcnt lgkmcnt(0)
	v_lshl_add_u64 v[34:35], s[0:1], 2, v[50:51]
	global_load_dwordx4 v[30:33], v[30:31], off offset:1024
	v_lshl_add_u64 v[42:43], v[34:35], 0, v[0:1]
	global_load_dwordx4 v[34:37], v[42:43], off
	global_load_dwordx4 v[38:41], v[42:43], off offset:1024
	v_lshl_add_u64 v[42:43], s[0:1], 3, v[50:51]
	v_lshl_add_u64 v[52:53], v[42:43], 0, v[0:1]
	global_load_dwordx4 v[42:45], v[52:53], off
	global_load_dwordx4 v[46:49], v[52:53], off offset:1024
	v_mad_u64_u32 v[52:53], s[16:17], s0, 12, v[50:51]
	v_mad_u64_u32 v[56:57], s[16:17], s0, 20, v[50:51]
	v_mad_u64_u32 v[62:63], s[16:17], s0, 24, v[50:51]
	v_lshl_add_u64 v[54:55], s[0:1], 4, v[50:51]
	v_mad_u64_u32 v[50:51], s[16:17], s0, 28, v[50:51]
	v_lshl_add_u64 v[54:55], v[54:55], 0, v[0:1]
	v_lshlrev_b64 v[6:7], 11, v[6:7]
	v_lshl_add_u64 v[6:7], s[18:19], 0, v[6:7]
	v_lshl_add_u64 v[6:7], v[6:7], 0, v[0:1]
	v_lshl_add_u64 v[4:5], s[4:5], 0, v[4:5]
	v_lshlrev_b64 v[2:3], 10, v[2:3]
	s_waitcnt vmcnt(8)
	v_pk_add_f32 v[58:59], v[14:15], v[10:11]
	v_mov_b32_e32 v10, v53
	v_pk_add_f32 v[60:61], v[16:17], v[12:13]
	v_mov_b32_e32 v12, v57
	v_mad_u64_u32 v[10:11], s[16:17], s1, 12, v[10:11]
	v_mov_b32_e32 v53, v10
	v_mov_b32_e32 v10, v63
	v_mad_u64_u32 v[12:13], s[16:17], s1, 20, v[12:13]
	v_mov_b32_e32 v57, v12
	v_mov_b32_e32 v12, v51
	v_mad_u64_u32 v[10:11], s[16:17], s1, 24, v[10:11]
	s_waitcnt vmcnt(6)
	v_pk_add_f32 v[66:67], v[18:19], v[22:23]
	v_lshl_add_u64 v[22:23], v[52:53], 0, v[0:1]
	v_mad_u64_u32 v[64:65], s[0:1], s1, 28, v[12:13]
	v_mov_b32_e32 v63, v10
	v_pk_add_f32 v[68:69], v[20:21], v[24:25]
	global_load_dwordx4 v[10:13], v[54:55], off
	global_load_dwordx4 v[14:17], v[54:55], off offset:1024
	global_load_dwordx4 v[18:21], v[22:23], off
	v_lshl_add_u64 v[52:53], v[56:57], 0, v[0:1]
	s_waitcnt vmcnt(8)
	v_pk_add_f32 v[54:55], v[58:59], v[26:27]
	v_pk_add_f32 v[56:57], v[60:61], v[28:29]
	global_load_dwordx4 v[26:29], v[52:53], off
	v_lshl_add_u64 v[58:59], v[62:63], 0, v[0:1]
	global_load_dwordx4 v[22:25], v[22:23], off offset:1024
	v_mov_b32_e32 v51, v64
	s_waitcnt vmcnt(9)
	v_pk_add_f32 v[60:61], v[66:67], v[30:31]
	v_pk_add_f32 v[62:63], v[68:69], v[32:33]
	s_waitcnt vmcnt(8)
	v_pk_add_f32 v[54:55], v[54:55], v[34:35]
	v_pk_add_f32 v[56:57], v[56:57], v[36:37]
	global_load_dwordx4 v[30:33], v[52:53], off offset:1024
	global_load_dwordx4 v[34:37], v[58:59], off
	v_lshl_add_u64 v[50:51], v[50:51], 0, v[0:1]
	s_waitcnt vmcnt(9)
	v_pk_add_f32 v[52:53], v[60:61], v[38:39]
	v_pk_add_f32 v[60:61], v[62:63], v[40:41]
	s_waitcnt vmcnt(8)
	v_pk_add_f32 v[54:55], v[54:55], v[42:43]
	v_pk_add_f32 v[56:57], v[56:57], v[44:45]
	global_load_dwordx4 v[38:41], v[50:51], off
	global_load_dwordx4 v[42:45], v[58:59], off offset:1024
	s_waitcnt vmcnt(9)
	v_pk_add_f32 v[52:53], v[52:53], v[46:47]
	v_pk_add_f32 v[58:59], v[60:61], v[48:49]
	global_load_dwordx4 v[46:49], v[50:51], off offset:1024
	s_waitcnt vmcnt(7)
	v_pk_add_f32 v[18:19], v[54:55], v[18:19]
	s_nop 0
	v_pk_add_f32 v[10:11], v[18:19], v[10:11]
	v_pk_add_f32 v[20:21], v[56:57], v[20:21]
	v_mov_b32_e32 v57, 0x3727c5ac
	s_waitcnt vmcnt(6)
	v_pk_add_f32 v[18:19], v[10:11], v[26:27]
	v_pk_add_f32 v[12:13], v[20:21], v[12:13]
	s_waitcnt vmcnt(5)
	v_pk_add_f32 v[22:23], v[52:53], v[22:23]
	v_pk_add_f32 v[10:11], v[58:59], v[24:25]
	v_pk_add_f32 v[14:15], v[22:23], v[14:15]
	v_pk_add_f32 v[10:11], v[10:11], v[16:17]
	v_pk_add_f32 v[20:21], v[12:13], v[28:29]
	v_mov_b32_e32 v58, 0x260
	s_waitcnt vmcnt(4)
	v_pk_add_f32 v[50:51], v[14:15], v[30:31]
	v_pk_add_f32 v[52:53], v[10:11], v[32:33]
	global_load_dwordx4 v[10:13], v0, s[12:13]
	global_load_dwordx4 v[14:17], v0, s[14:15]
	s_waitcnt vmcnt(5)
	v_pk_add_f32 v[18:19], v[18:19], v[34:35]
	s_waitcnt vmcnt(4)
	v_pk_add_f32 v[34:35], v[18:19], v[38:39]
	v_pk_add_f32 v[18:19], v[20:21], v[36:37]
	v_add_f32_e32 v9, 0, v34
	v_pk_add_f32 v[36:37], v[18:19], v[40:41]
	global_load_dwordx4 v[18:21], v0, s[12:13] offset:1024
	global_load_dwordx4 v[22:25], v0, s[14:15] offset:1024
	global_load_dwordx4 v[26:29], v[6:7], off
	global_load_dwordx4 v[30:33], v[6:7], off offset:1024
	v_add_f32_e32 v9, v9, v35
	v_add_f32_e32 v9, v9, v36
	s_waitcnt vmcnt(7)
	v_pk_add_f32 v[6:7], v[50:51], v[42:43]
	v_add_f32_e32 v9, v9, v37
	s_waitcnt vmcnt(6)
	v_pk_add_f32 v[6:7], v[6:7], v[46:47]
	v_pk_add_f32 v[38:39], v[52:53], v[44:45]
	v_add_f32_e32 v9, v9, v6
	v_add_f32_e32 v9, v9, v7
	v_pk_add_f32 v[38:39], v[38:39], v[48:49]
	s_nop 0
	v_add_f32_e32 v9, v9, v38
	v_add_f32_e32 v9, v9, v39
	s_nop 1
	v_add_f32_dpp v9, v9, v9 quad_perm:[1,0,3,2] row_mask:0xf bank_mask:0xf bound_ctrl:1
	s_nop 1
	v_add_f32_dpp v9, v9, v9 quad_perm:[2,3,0,1] row_mask:0xf bank_mask:0xf bound_ctrl:1
	s_nop 1
	v_add_f32_dpp v9, v9, v9 row_half_mirror row_mask:0xf bank_mask:0xf bound_ctrl:1
	s_nop 1
	v_add_f32_dpp v9, v9, v9 row_mirror row_mask:0xf bank_mask:0xf bound_ctrl:1
	s_nop 0
	v_readlane_b32 s12, v9, 16
	v_readlane_b32 s13, v9, 48
	v_readlane_b32 s0, v9, 0
	v_readlane_b32 s1, v9, 32
	v_mov_b32_e32 v40, s12
	v_mov_b32_e32 v41, s13
	v_pk_add_f32 v[40:41], s[0:1], v[40:41]
	s_nop 0
	v_add_f32_e32 v9, v40, v41
	v_mul_f32_e32 v40, 0x3b000000, v9
	v_pk_add_f32 v[50:51], v[34:35], v[40:41] op_sel_hi:[1,0] neg_lo:[0,1] neg_hi:[0,1]
	v_pk_add_f32 v[52:53], v[36:37], v[40:41] op_sel_hi:[1,0] neg_lo:[0,1] neg_hi:[0,1]
	v_pk_mul_f32 v[34:35], v[50:51], v[50:51]
	v_pk_mul_f32 v[36:37], v[52:53], v[52:53]
	v_add_f32_e32 v9, v34, v35
	v_pk_add_f32 v[6:7], v[6:7], v[40:41] op_sel_hi:[1,0] neg_lo:[0,1] neg_hi:[0,1]
	v_add_f32_e32 v9, v9, v36
	v_pk_mul_f32 v[42:43], v[6:7], v[6:7]
	v_add_f32_e32 v9, v9, v37
	v_pk_add_f32 v[54:55], v[38:39], v[40:41] op_sel_hi:[1,0] neg_lo:[0,1] neg_hi:[0,1]
	v_add_f32_e32 v9, v9, v42
	v_pk_mul_f32 v[38:39], v[54:55], v[54:55]
	v_add_f32_e32 v9, v9, v43
	v_add_f32_e32 v9, v9, v38
	v_add_f32_e32 v9, v9, v39
	s_waitcnt vmcnt(5)
	v_pk_mul_f32 v[10:11], v[10:11], v[50:51]
	v_add_f32_dpp v9, v9, v9 quad_perm:[1,0,3,2] row_mask:0xf bank_mask:0xf bound_ctrl:1
	v_pk_mul_f32 v[12:13], v[12:13], v[52:53]
	s_waitcnt vmcnt(3)
	v_pk_mul_f32 v[6:7], v[18:19], v[6:7]
	v_add_f32_dpp v9, v9, v9 quad_perm:[2,3,0,1] row_mask:0xf bank_mask:0xf bound_ctrl:1
	s_nop 1
	v_add_f32_dpp v9, v9, v9 row_half_mirror row_mask:0xf bank_mask:0xf bound_ctrl:1
	s_nop 1
	v_add_f32_dpp v9, v9, v9 row_mirror row_mask:0xf bank_mask:0xf bound_ctrl:1
	s_nop 0
	v_readlane_b32 s12, v9, 16
	v_readlane_b32 s13, v9, 48
	v_readlane_b32 s0, v9, 0
	v_readlane_b32 s1, v9, 32
	v_mov_b32_e32 v34, s12
	v_mov_b32_e32 v35, s13
	v_pk_add_f32 v[34:35], s[0:1], v[34:35]
	s_mov_b32 s12, 0xf800000
	v_add_f32_e32 v9, v34, v35
	v_fmamk_f32 v9, v9, 0x3b000000, v57
	v_mul_f32_e32 v34, 0x4f800000, v9
	v_cmp_gt_f32_e32 vcc, s12, v9
	s_nop 1
	v_cndmask_b32_e32 v9, v9, v34, vcc
	v_sqrt_f32_e32 v34, v9
	s_nop 0
	v_add_u32_e32 v35, -1, v34
	v_fma_f32 v36, -v35, v34, v9
	v_cmp_ge_f32_e64 s[0:1], 0, v36
	v_add_u32_e32 v36, 1, v34
	s_nop 0
	v_cndmask_b32_e64 v35, v34, v35, s[0:1]
	v_fma_f32 v34, -v36, v34, v9
	v_cmp_lt_f32_e64 s[0:1], 0, v34
	s_nop 1
	v_cndmask_b32_e64 v34, v35, v36, s[0:1]
	v_mul_f32_e32 v35, 0x37800000, v34
	v_cndmask_b32_e32 v34, v34, v35, vcc
	v_cmp_class_f32_e32 vcc, v9, v58
	s_nop 1
	v_cndmask_b32_e32 v9, v34, v9, vcc
	v_div_scale_f32 v42, s[0:1], v9, v9, 1.0
	v_rcp_f32_e32 v43, v42
	global_load_dwordx4 v[34:37], v0, s[8:9]
	global_load_dwordx4 v[38:41], v0, s[10:11]
	v_fma_f32 v44, -v42, v43, 1.0
	v_fmac_f32_e32 v43, v44, v43
	v_div_scale_f32 v44, vcc, 1.0, v9, 1.0
	v_mul_f32_e32 v45, v44, v43
	v_fma_f32 v46, -v42, v45, v44
	v_fmac_f32_e32 v45, v46, v43
	v_fma_f32 v42, -v42, v45, v44
	v_div_fmas_f32 v56, v42, v43, v45
	global_load_dwordx4 v[42:45], v0, s[8:9] offset:1024
	global_load_dwordx4 v[46:49], v0, s[10:11] offset:1024
	v_div_fixup_f32 v56, v56, v9, 1.0
	v_pk_fma_f32 v[10:11], v[56:57], v[10:11], v[14:15] op_sel_hi:[0,1,1]
	s_waitcnt vmcnt(5)
	v_pk_add_f32 v[10:11], v[10:11], v[26:27]
	v_pk_fma_f32 v[12:13], v[56:57], v[12:13], v[16:17] op_sel_hi:[0,1,1]
	v_add_f32_e32 v9, 0, v10
	v_add_f32_e32 v9, v9, v11
	v_pk_add_f32 v[12:13], v[12:13], v[28:29]
	v_pk_fma_f32 v[6:7], v[56:57], v[6:7], v[22:23] op_sel_hi:[0,1,1]
	v_add_f32_e32 v9, v9, v12
	v_pk_mul_f32 v[14:15], v[20:21], v[54:55]
	v_add_f32_e32 v9, v9, v13
	s_waitcnt vmcnt(4)
	v_pk_add_f32 v[6:7], v[6:7], v[30:31]
	v_pk_fma_f32 v[14:15], v[56:57], v[14:15], v[24:25] op_sel_hi:[0,1,1]
	v_add_f32_e32 v9, v9, v6
	v_add_f32_e32 v9, v9, v7
	v_pk_add_f32 v[14:15], v[14:15], v[32:33]
	s_nop 0
	v_add_f32_e32 v9, v9, v14
	v_add_f32_e32 v9, v9, v15
	s_nop 1
	v_add_f32_dpp v9, v9, v9 quad_perm:[1,0,3,2] row_mask:0xf bank_mask:0xf bound_ctrl:1
	s_nop 1
	v_add_f32_dpp v9, v9, v9 quad_perm:[2,3,0,1] row_mask:0xf bank_mask:0xf bound_ctrl:1
	s_nop 1
	v_add_f32_dpp v9, v9, v9 row_half_mirror row_mask:0xf bank_mask:0xf bound_ctrl:1
	s_nop 1
	v_add_f32_dpp v9, v9, v9 row_mirror row_mask:0xf bank_mask:0xf bound_ctrl:1
	s_nop 0
	v_readlane_b32 s8, v9, 16
	v_readlane_b32 s9, v9, 48
	v_readlane_b32 s0, v9, 0
	v_readlane_b32 s1, v9, 32
	v_mov_b32_e32 v16, s8
	v_mov_b32_e32 v17, s9
	v_pk_add_f32 v[16:17], s[0:1], v[16:17]
	s_nop 0
	v_add_f32_e32 v9, v16, v17
	v_mul_f32_e32 v16, 0x3b000000, v9
	v_pk_add_f32 v[10:11], v[10:11], v[16:17] op_sel_hi:[1,0] neg_lo:[0,1] neg_hi:[0,1]
	v_pk_add_f32 v[12:13], v[12:13], v[16:17] op_sel_hi:[1,0] neg_lo:[0,1] neg_hi:[0,1]
	v_pk_mul_f32 v[18:19], v[10:11], v[10:11]
	v_pk_mul_f32 v[20:21], v[12:13], v[12:13]
	v_add_f32_e32 v9, v18, v19
	v_pk_add_f32 v[22:23], v[6:7], v[16:17] op_sel_hi:[1,0] neg_lo:[0,1] neg_hi:[0,1]
	v_add_f32_e32 v9, v9, v20
	v_pk_mul_f32 v[6:7], v[22:23], v[22:23]
	v_add_f32_e32 v9, v9, v21
	v_pk_add_f32 v[14:15], v[14:15], v[16:17] op_sel_hi:[1,0] neg_lo:[0,1] neg_hi:[0,1]
	v_add_f32_e32 v6, v9, v6
	v_pk_mul_f32 v[16:17], v[14:15], v[14:15]
	v_add_f32_e32 v6, v6, v7
	v_add_f32_e32 v6, v6, v16
	v_add_f32_e32 v6, v6, v17
	s_nop 1
	v_add_f32_dpp v6, v6, v6 quad_perm:[1,0,3,2] row_mask:0xf bank_mask:0xf bound_ctrl:1
	s_nop 1
	v_add_f32_dpp v6, v6, v6 quad_perm:[2,3,0,1] row_mask:0xf bank_mask:0xf bound_ctrl:1
	s_nop 1
	v_add_f32_dpp v6, v6, v6 row_half_mirror row_mask:0xf bank_mask:0xf bound_ctrl:1
	s_nop 1
	v_add_f32_dpp v6, v6, v6 row_mirror row_mask:0xf bank_mask:0xf bound_ctrl:1
	s_nop 0
	v_readlane_b32 s8, v6, 16
	v_readlane_b32 s9, v6, 48
	v_readlane_b32 s0, v6, 0
	v_readlane_b32 s1, v6, 32
	v_mov_b32_e32 v6, s8
	v_mov_b32_e32 v7, s9
	v_pk_add_f32 v[6:7], s[0:1], v[6:7]
	s_nop 0
	v_add_f32_e32 v6, v6, v7
	v_fmac_f32_e32 v57, 0x3b000000, v6
	v_mul_f32_e32 v6, 0x4f800000, v57
	v_cmp_gt_f32_e32 vcc, s12, v57
	s_nop 1
	v_cndmask_b32_e32 v6, v57, v6, vcc
	v_sqrt_f32_e32 v7, v6
	s_nop 0
	v_add_u32_e32 v9, -1, v7
	v_fma_f32 v16, -v9, v7, v6
	v_cmp_ge_f32_e64 s[0:1], 0, v16
	v_add_u32_e32 v16, 1, v7
	s_nop 0
	v_cndmask_b32_e64 v9, v7, v9, s[0:1]
	v_fma_f32 v7, -v16, v7, v6
	v_cmp_lt_f32_e64 s[0:1], 0, v7
	s_nop 1
	v_cndmask_b32_e64 v7, v9, v16, s[0:1]
	v_mul_f32_e32 v9, 0x37800000, v7
	v_cndmask_b32_e32 v7, v7, v9, vcc
	v_cmp_class_f32_e32 vcc, v6, v58
	v_lshl_add_u64 v[16:17], v[4:5], 0, v[0:1]
	s_nop 0
	v_cndmask_b32_e32 v6, v7, v6, vcc
	v_div_scale_f32 v7, s[0:1], v6, v6, 1.0
	v_rcp_f32_e32 v9, v7
	s_mov_b32 s0, 0x43000000
	v_fma_f32 v0, -v7, v9, 1.0
	v_fmac_f32_e32 v9, v0, v9
	v_div_scale_f32 v0, vcc, 1.0, v6, 1.0
	v_mul_f32_e32 v4, v0, v9
	v_fma_f32 v5, -v7, v4, v0
	v_fmac_f32_e32 v4, v5, v9
	v_fma_f32 v0, -v7, v4, v0
	v_div_fmas_f32 v0, v0, v9, v4
	v_div_fixup_f32 v0, v0, v6, 1.0
	s_waitcnt vmcnt(3)
	v_pk_mul_f32 v[4:5], v[34:35], v[10:11]
	v_pk_mul_f32 v[6:7], v[36:37], v[12:13]
	s_waitcnt vmcnt(2)
	v_pk_fma_f32 v[4:5], v[0:1], v[4:5], v[38:39] op_sel_hi:[0,1,1]
	v_pk_fma_f32 v[6:7], v[0:1], v[6:7], v[40:41] op_sel_hi:[0,1,1]
	s_waitcnt vmcnt(1)
	v_pk_mul_f32 v[10:11], v[42:43], v[22:23]
	v_pk_mul_f32 v[12:13], v[44:45], v[14:15]
	v_fma_mixlo_f16 v9, v4, s0, 0
	s_waitcnt vmcnt(0)
	v_pk_fma_f32 v[10:11], v[0:1], v[10:11], v[46:47] op_sel_hi:[0,1,1]
	v_pk_fma_f32 v[12:13], v[0:1], v[12:13], v[48:49] op_sel_hi:[0,1,1]
	global_store_dwordx4 v[16:17], v[4:7], off sc1
	global_store_dwordx4 v[16:17], v[10:13], off offset:1024 sc1
	v_mul_f32_e32 v0, 0x43000000, v4
	v_fma_mixlo_f16 v4, v4, s0, -v9 op_sel_hi:[0,0,1]
	v_fma_mixlo_f16 v15, v5, s0, 0
	v_pk_mul_f32 v[18:19], v[6:7], s[0:1] op_sel_hi:[1,0]
	v_fma_mixhi_f16 v4, v5, s0, -v15 op_sel_hi:[0,0,1]
	v_cvt_pk_f16_f32 v15, v18, v19
	v_pk_mul_f32 v[20:21], v[12:13], s[0:1] op_sel_hi:[1,0]
	v_cvt_f32_f16_e32 v18, v15
	v_cvt_f32_f16_sdwa v19, v15 dst_sel:DWORD dst_unused:UNUSED_PAD src0_sel:WORD_1
	v_cvt_pk_f16_f32 v17, v20, v21
	v_cvt_f32_f16_e32 v20, v17
	v_cvt_f32_f16_sdwa v21, v17 dst_sel:DWORD dst_unused:UNUSED_PAD src0_sel:WORD_1
	v_fma_mixlo_f16 v14, v10, s0, 0
	v_mul_f32_e32 v9, 0x43000000, v10
	v_fma_mixlo_f16 v10, v10, s0, -v14 op_sel_hi:[0,0,1]
	v_mul_f32_e32 v14, 0x43000000, v5
	v_fma_mixlo_f16 v5, v11, s0, 0
	v_pk_fma_f32 v[6:7], v[6:7], s[0:1], v[18:19] op_sel_hi:[1,0,1] neg_lo:[0,0,1] neg_hi:[0,0,1]
	v_cvt_pk_f16_f32 v14, v0, v14
	v_mul_f32_e32 v0, 0x43000000, v11
	v_fma_mixhi_f16 v10, v11, s0, -v5 op_sel_hi:[0,0,1]
	v_cvt_pk_f16_f32 v5, v6, v7
	v_pk_fma_f32 v[6:7], v[12:13], s[0:1], v[20:21] op_sel_hi:[1,0,1] neg_lo:[0,0,1] neg_hi:[0,0,1]
	v_cvt_pk_f16_f32 v16, v9, v0
	v_cvt_pk_f16_f32 v11, v6, v7
	v_lshl_add_u64 v[6:7], s[6:7], 0, v[2:3]
	v_lshlrev_b32_e32 v0, 1, v8
	v_lshl_add_u64 v[2:3], s[2:3], 0, v[2:3]
	v_lshl_add_u64 v[6:7], v[6:7], 0, v[0:1]
	v_lshl_add_u64 v[0:1], v[2:3], 0, v[0:1]
	v_mbcnt_lo_u32_b32 v20, -1, 0
	v_mbcnt_hi_u32_b32 v20, -1, v20
	v_and_b32_e32 v20, 1, v20
	v_cmp_eq_u32_e32 vcc, 1, v20
	v_mul_u32_u24_e32 v22, 0x1f8, v20
	v_mov_b32_e32 v23, 0
	s_nop 1
	v_mov_b32_dpp v24, v14 quad_perm:[1,0,3,2] row_mask:0xf bank_mask:0xf
	v_mov_b32_dpp v25, v15 quad_perm:[1,0,3,2] row_mask:0xf bank_mask:0xf
	v_mov_b32_dpp v26, v16 quad_perm:[1,0,3,2] row_mask:0xf bank_mask:0xf
	v_mov_b32_dpp v27, v17 quad_perm:[1,0,3,2] row_mask:0xf bank_mask:0xf
	s_nop 1
	v_cndmask_b32_e32 v28, v14, v26, vcc
	v_cndmask_b32_e32 v29, v15, v27, vcc
	v_cndmask_b32_e32 v30, v24, v16, vcc
	v_cndmask_b32_e32 v31, v25, v17, vcc
	v_lshl_add_u64 v[32:33], v[6:7], 0, v[22:23]
	global_store_dwordx4 v[32:33], v[28:31], off sc1
	s_nop 1
	v_mov_b32_dpp v24, v4 quad_perm:[1,0,3,2] row_mask:0xf bank_mask:0xf
	v_mov_b32_dpp v25, v5 quad_perm:[1,0,3,2] row_mask:0xf bank_mask:0xf
	v_mov_b32_dpp v26, v10 quad_perm:[1,0,3,2] row_mask:0xf bank_mask:0xf
	v_mov_b32_dpp v27, v11 quad_perm:[1,0,3,2] row_mask:0xf bank_mask:0xf
	s_nop 1
	v_cndmask_b32_e32 v28, v4, v26, vcc
	v_cndmask_b32_e32 v29, v5, v27, vcc
	v_cndmask_b32_e32 v30, v24, v10, vcc
	v_cndmask_b32_e32 v31, v25, v11, vcc
	v_lshl_add_u64 v[32:33], v[0:1], 0, v[22:23]
	global_store_dwordx4 v[32:33], v[28:31], off sc1
	s_nop 1
	s_endpgm
	s_endpgm
	s_endpgm
	s_endpgm
	s_endpgm
	s_endpgm
	s_endpgm
	s_endpgm
	s_endpgm
	s_endpgm
	s_endpgm
	s_endpgm
	s_endpgm
	s_endpgm
	s_endpgm
	s_endpgm
	s_endpgm
	s_endpgm
	s_endpgm
	s_endpgm
	s_endpgm
	s_endpgm
	s_endpgm
	s_endpgm
	s_endpgm
	s_endpgm
	s_endpgm
	s_endpgm
	s_endpgm
	s_endpgm
	s_endpgm
	s_endpgm
	s_endpgm
	s_endpgm
	s_endpgm
	s_endpgm
	s_endpgm
	s_endpgm
	s_endpgm
	s_endpgm
	s_endpgm
	s_endpgm
	s_endpgm
	s_endpgm
	s_endpgm
	s_endpgm
	s_endpgm
	s_endpgm
	s_endpgm
	s_endpgm
	s_endpgm
	s_endpgm
	s_endpgm
	s_endpgm
	s_endpgm

.LBB20_5:
	v_lshlrev_b32_e32 v0, 2, v0
	v_and_b32_e32 v54, 0xfc, v0
	v_lshlrev_b64 v[44:45], 11, v[2:3]
	v_lshlrev_b64 v[4:5], 11, v[4:5]
	s_waitcnt lgkmcnt(0)
	v_lshl_add_u64 v[24:25], s[18:19], 0, v[44:45]
	v_lshlrev_b32_e32 v0, 2, v54
	v_mov_b32_e32 v1, 0
	v_lshl_add_u64 v[4:5], s[14:15], 0, v[4:5]
	v_lshl_add_u64 v[20:21], v[4:5], 0, v[0:1]
	v_lshl_add_u64 v[26:27], v[24:25], 0, v[0:1]
	global_load_dwordx4 v[4:7], v[20:21], off
	global_load_dwordx4 v[8:11], v0, s[16:17]
	global_load_dwordx4 v[12:15], v0, s[16:17] offset:1024
	global_load_dwordx4 v[16:19], v[20:21], off offset:1024
	v_lshl_add_u64 v[28:29], s[0:1], 2, v[24:25]
	global_load_dwordx4 v[20:23], v[26:27], off
	v_lshl_add_u64 v[46:47], v[28:29], 0, v[0:1]
	global_load_dwordx4 v[24:27], v[26:27], off offset:1024
	s_nop 0
	global_load_dwordx4 v[28:31], v[46:47], off
	global_load_dwordx4 v[32:35], v[46:47], off offset:1024
	global_load_dwordx4 v[36:39], v0, s[8:9]
	global_load_dwordx4 v[40:43], v0, s[8:9] offset:1024
	v_lshl_add_u64 v[44:45], s[4:5], 0, v[44:45]
	v_lshl_add_u64 v[52:53], v[44:45], 0, v[0:1]
	global_load_dwordx4 v[44:47], v0, s[10:11]
	global_load_dwordx4 v[48:51], v0, s[10:11] offset:1024
	v_mov_b32_e32 v55, 0x3727c5ac
	s_mov_b32 s9, 0xf800000
	v_mov_b32_e32 v56, 0x260
	s_mov_b32 s8, 0x43000000
	v_lshlrev_b64 v[2:3], 10, v[2:3]
	s_waitcnt vmcnt(10)
	v_pk_add_f32 v[4:5], v[8:9], v[4:5]
	v_pk_add_f32 v[6:7], v[10:11], v[6:7]
	s_waitcnt vmcnt(8)
	v_pk_add_f32 v[8:9], v[12:13], v[16:17]
	v_pk_add_f32 v[10:11], v[14:15], v[18:19]
	s_waitcnt vmcnt(7)
	v_pk_add_f32 v[4:5], v[4:5], v[20:21]
	v_pk_add_f32 v[6:7], v[6:7], v[22:23]
	s_waitcnt vmcnt(5)
	v_pk_add_f32 v[4:5], v[4:5], v[28:29]
	v_pk_add_f32 v[6:7], v[6:7], v[30:31]
	v_add_f32_e32 v0, 0, v4
	v_add_f32_e32 v0, v0, v5
	v_pk_add_f32 v[8:9], v[8:9], v[24:25]
	v_add_f32_e32 v0, v0, v6
	s_waitcnt vmcnt(4)
	v_pk_add_f32 v[8:9], v[8:9], v[32:33]
	v_add_f32_e32 v0, v0, v7
	v_pk_add_f32 v[10:11], v[10:11], v[26:27]
	v_add_f32_e32 v0, v0, v8
	v_pk_add_f32 v[10:11], v[10:11], v[34:35]
	v_add_f32_e32 v0, v0, v9
	v_add_f32_e32 v0, v0, v10
	v_add_f32_e32 v0, v0, v11
	s_nop 1
	v_add_f32_dpp v0, v0, v0 quad_perm:[1,0,3,2] row_mask:0xf bank_mask:0xf bound_ctrl:1
	s_nop 1
	v_add_f32_dpp v0, v0, v0 quad_perm:[2,3,0,1] row_mask:0xf bank_mask:0xf bound_ctrl:1
	s_nop 1
	v_add_f32_dpp v0, v0, v0 row_half_mirror row_mask:0xf bank_mask:0xf bound_ctrl:1
	s_nop 1
	v_add_f32_dpp v0, v0, v0 row_mirror row_mask:0xf bank_mask:0xf bound_ctrl:1
	s_nop 0
	v_readlane_b32 s4, v0, 16
	v_readlane_b32 s5, v0, 48
	v_readlane_b32 s0, v0, 0
	v_readlane_b32 s1, v0, 32
	v_mov_b32_e32 v12, s4
	v_mov_b32_e32 v13, s5
	v_pk_add_f32 v[12:13], s[0:1], v[12:13]
	s_nop 0
	v_add_f32_e32 v0, v12, v13
	v_mul_f32_e32 v0, 0x3b000000, v0
	v_pk_add_f32 v[4:5], v[4:5], v[0:1] op_sel_hi:[1,0] neg_lo:[0,1] neg_hi:[0,1]
	v_pk_add_f32 v[6:7], v[6:7], v[0:1] op_sel_hi:[1,0] neg_lo:[0,1] neg_hi:[0,1]
	v_pk_mul_f32 v[12:13], v[4:5], v[4:5]
	v_pk_add_f32 v[8:9], v[8:9], v[0:1] op_sel_hi:[1,0] neg_lo:[0,1] neg_hi:[0,1]
	v_pk_add_f32 v[10:11], v[10:11], v[0:1] op_sel_hi:[1,0] neg_lo:[0,1] neg_hi:[0,1]
	v_pk_mul_f32 v[14:15], v[6:7], v[6:7]
	v_add_f32_e32 v0, v12, v13
	v_add_f32_e32 v0, v0, v14
	v_pk_mul_f32 v[16:17], v[8:9], v[8:9]
	v_add_f32_e32 v0, v0, v15
	v_add_f32_e32 v0, v0, v16
	v_pk_mul_f32 v[18:19], v[10:11], v[10:11]
	v_add_f32_e32 v0, v0, v17
	v_add_f32_e32 v0, v0, v18
	v_add_f32_e32 v0, v0, v19
	s_waitcnt vmcnt(3)
	v_pk_mul_f32 v[6:7], v[38:39], v[6:7]
	s_waitcnt vmcnt(2)
	v_pk_mul_f32 v[8:9], v[40:41], v[8:9]
	v_add_f32_dpp v0, v0, v0 quad_perm:[1,0,3,2] row_mask:0xf bank_mask:0xf bound_ctrl:1
	v_pk_mul_f32 v[4:5], v[36:37], v[4:5]
	v_pk_mul_f32 v[10:11], v[42:43], v[10:11]
	v_add_f32_dpp v0, v0, v0 quad_perm:[2,3,0,1] row_mask:0xf bank_mask:0xf bound_ctrl:1
	s_nop 1
	v_add_f32_dpp v0, v0, v0 row_half_mirror row_mask:0xf bank_mask:0xf bound_ctrl:1
	s_nop 1
	v_add_f32_dpp v0, v0, v0 row_mirror row_mask:0xf bank_mask:0xf bound_ctrl:1
	s_nop 0
	v_readlane_b32 s4, v0, 16
	v_readlane_b32 s5, v0, 48
	v_readlane_b32 s0, v0, 0
	v_readlane_b32 s1, v0, 32
	v_mov_b32_e32 v12, s4
	v_mov_b32_e32 v13, s5
	v_pk_add_f32 v[12:13], s[0:1], v[12:13]
	s_nop 0
	v_add_f32_e32 v0, v12, v13
	v_fmac_f32_e32 v55, 0x3b000000, v0
	v_mul_f32_e32 v0, 0x4f800000, v55
	v_cmp_gt_f32_e32 vcc, s9, v55
	s_nop 1
	v_cndmask_b32_e32 v0, v55, v0, vcc
	v_sqrt_f32_e32 v12, v0
	s_nop 0
	v_add_u32_e32 v13, -1, v12
	v_add_u32_e32 v14, 1, v12
	v_fma_f32 v15, -v13, v12, v0
	v_fma_f32 v16, -v14, v12, v0
	v_cmp_ge_f32_e64 s[0:1], 0, v15
	s_nop 1
	v_cndmask_b32_e64 v12, v12, v13, s[0:1]
	v_cmp_lt_f32_e64 s[0:1], 0, v16
	s_nop 1
	v_cndmask_b32_e64 v12, v12, v14, s[0:1]
	v_mul_f32_e32 v13, 0x37800000, v12
	v_cndmask_b32_e32 v12, v12, v13, vcc
	v_cmp_class_f32_e32 vcc, v0, v56
	s_nop 1
	v_cndmask_b32_e32 v0, v12, v0, vcc
	v_div_scale_f32 v12, s[0:1], v0, v0, 1.0
	v_rcp_f32_e32 v13, v12
	v_div_scale_f32 v14, vcc, 1.0, v0, 1.0
	v_fma_f32 v15, -v12, v13, 1.0
	v_fmac_f32_e32 v13, v15, v13
	v_mul_f32_e32 v15, v14, v13
	v_fma_f32 v16, -v12, v15, v14
	v_fmac_f32_e32 v15, v16, v13
	v_fma_f32 v12, -v12, v15, v14
	v_div_fmas_f32 v12, v12, v13, v15
	v_div_fixup_f32 v0, v12, v0, 1.0
	s_waitcnt vmcnt(1)
	v_pk_fma_f32 v[6:7], v[0:1], v[6:7], v[46:47] op_sel_hi:[0,1,1]
	s_waitcnt vmcnt(0)
	v_pk_fma_f32 v[8:9], v[0:1], v[8:9], v[48:49] op_sel_hi:[0,1,1]
	v_pk_fma_f32 v[4:5], v[0:1], v[4:5], v[44:45] op_sel_hi:[0,1,1]
	v_mul_f32_e32 v17, 0x43000000, v8
	v_fma_mixlo_f16 v18, v8, s8, 0
	v_mul_f32_e32 v21, 0x43000000, v9
	v_pk_mul_f32 v[12:13], v[6:7], s[8:9] op_sel_hi:[1,0]
	v_pk_fma_f32 v[10:11], v[0:1], v[10:11], v[50:51] op_sel_hi:[0,1,1]
	global_store_dwordx4 v[52:53], v[4:7], off sc1
	global_store_dwordx4 v[52:53], v[8:11], off offset:1024 sc1
	v_mul_f32_e32 v0, 0x43000000, v4
	v_fma_mixlo_f16 v16, v4, s8, 0
	v_fma_mixlo_f16 v8, v8, s8, -v18 op_sel_hi:[0,0,1]
	v_cvt_pk_f16_f32 v18, v17, v21
	v_cvt_pk_f16_f32 v17, v12, v13
	v_mul_f32_e32 v19, 0x43000000, v5
	v_pk_mul_f32 v[14:15], v[10:11], s[8:9] op_sel_hi:[1,0]
	v_cvt_f32_f16_e32 v12, v17
	v_cvt_f32_f16_sdwa v13, v17 dst_sel:DWORD dst_unused:UNUSED_PAD src0_sel:WORD_1
	v_fma_mixlo_f16 v4, v4, s8, -v16 op_sel_hi:[0,0,1]
	v_cvt_pk_f16_f32 v16, v0, v19
	v_cvt_pk_f16_f32 v19, v14, v15
	v_cvt_f32_f16_e32 v14, v19
	v_cvt_f32_f16_sdwa v15, v19 dst_sel:DWORD dst_unused:UNUSED_PAD src0_sel:WORD_1
	v_fma_mixlo_f16 v20, v5, s8, 0
	v_pk_fma_f32 v[6:7], v[6:7], s[8:9], v[12:13] op_sel_hi:[1,0,1] neg_lo:[0,0,1] neg_hi:[0,0,1]
	v_fma_mixhi_f16 v4, v5, s8, -v20 op_sel_hi:[0,0,1]
	v_cvt_pk_f16_f32 v5, v6, v7
	v_lshl_add_u64 v[6:7], s[6:7], 0, v[2:3]
	v_lshlrev_b32_e32 v0, 1, v54
	v_lshl_add_u64 v[2:3], s[2:3], 0, v[2:3]
	v_fma_mixlo_f16 v22, v9, s8, 0
	v_pk_fma_f32 v[10:11], v[10:11], s[8:9], v[14:15] op_sel_hi:[1,0,1] neg_lo:[0,0,1] neg_hi:[0,0,1]
	v_lshl_add_u64 v[6:7], v[6:7], 0, v[0:1]
	v_lshl_add_u64 v[0:1], v[2:3], 0, v[0:1]
	v_fma_mixhi_f16 v8, v9, s8, -v22 op_sel_hi:[0,0,1]
	v_cvt_pk_f16_f32 v9, v10, v11
	v_mbcnt_lo_u32_b32 v20, -1, 0
	v_mbcnt_hi_u32_b32 v20, -1, v20
	v_and_b32_e32 v20, 1, v20
	v_cmp_eq_u32_e32 vcc, 1, v20
	v_mul_u32_u24_e32 v22, 0x1f8, v20
	v_mov_b32_e32 v23, 0
	s_nop 1
	v_mov_b32_dpp v24, v16 quad_perm:[1,0,3,2] row_mask:0xf bank_mask:0xf
	v_mov_b32_dpp v25, v17 quad_perm:[1,0,3,2] row_mask:0xf bank_mask:0xf
	v_mov_b32_dpp v26, v18 quad_perm:[1,0,3,2] row_mask:0xf bank_mask:0xf
	v_mov_b32_dpp v27, v19 quad_perm:[1,0,3,2] row_mask:0xf bank_mask:0xf
	s_nop 1
	v_cndmask_b32_e32 v28, v16, v26, vcc
	v_cndmask_b32_e32 v29, v17, v27, vcc
	v_cndmask_b32_e32 v30, v24, v18, vcc
	v_cndmask_b32_e32 v31, v25, v19, vcc
	v_lshl_add_u64 v[32:33], v[6:7], 0, v[22:23]
	global_store_dwordx4 v[32:33], v[28:31], off sc1
	s_nop 1
	v_mov_b32_dpp v24, v4 quad_perm:[1,0,3,2] row_mask:0xf bank_mask:0xf
	v_mov_b32_dpp v25, v5 quad_perm:[1,0,3,2] row_mask:0xf bank_mask:0xf
	v_mov_b32_dpp v26, v8 quad_perm:[1,0,3,2] row_mask:0xf bank_mask:0xf
	v_mov_b32_dpp v27, v9 quad_perm:[1,0,3,2] row_mask:0xf bank_mask:0xf
	s_nop 1
	v_cndmask_b32_e32 v28, v4, v26, vcc
	v_cndmask_b32_e32 v29, v5, v27, vcc
	v_cndmask_b32_e32 v30, v24, v8, vcc
	v_cndmask_b32_e32 v31, v25, v9, vcc
	v_lshl_add_u64 v[32:33], v[0:1], 0, v[22:23]
	global_store_dwordx4 v[32:33], v[28:31], off sc1
	s_nop 1
	s_endpgm
	s_endpgm
	s_endpgm
	s_endpgm
	s_endpgm
	s_endpgm
	s_endpgm
	s_endpgm
	s_endpgm
	s_endpgm
	s_endpgm
	s_endpgm
	s_endpgm
	s_endpgm
	s_endpgm
	s_endpgm

.LBB21_5:
	v_lshlrev_b32_e32 v0, 2, v0
	v_and_b32_e32 v58, 0xfc, v0
	v_lshlrev_b64 v[4:5], 11, v[4:5]
	v_lshlrev_b32_e32 v0, 2, v58
	v_mov_b32_e32 v1, 0
	s_waitcnt lgkmcnt(0)
	v_lshl_add_u64 v[4:5], s[18:19], 0, v[4:5]
	v_lshl_add_u64 v[20:21], v[4:5], 0, v[0:1]
	global_load_dwordx4 v[4:7], v[20:21], off
	global_load_dwordx4 v[8:11], v0, s[16:17]
	global_load_dwordx4 v[12:15], v0, s[16:17] offset:1024
	global_load_dwordx4 v[16:19], v[20:21], off offset:1024
	v_lshlrev_b64 v[52:53], 11, v[2:3]
	v_lshl_add_u64 v[28:29], s[14:15], 0, v[52:53]
	v_lshl_add_u64 v[24:25], v[28:29], 0, v[0:1]
	v_mov_b32_e32 v59, 0x3727c5ac
	s_waitcnt lgkmcnt(0)
	v_lshl_add_u64 v[20:21], s[0:1], 2, v[28:29]
	v_lshl_add_u64 v[26:27], s[0:1], 3, v[28:29]
	v_lshl_add_u64 v[36:37], v[20:21], 0, v[0:1]
	global_load_dwordx4 v[20:23], v[24:25], off
	v_lshl_add_u64 v[40:41], v[26:27], 0, v[0:1]
	global_load_dwordx4 v[24:27], v[24:25], off offset:1024
	v_mad_u64_u32 v[44:45], s[12:13], s0, 12, v[28:29]
	v_mov_b32_e32 v38, v45
	v_mad_u64_u32 v[42:43], s[0:1], s1, 12, v[38:39]
	global_load_dwordx4 v[28:31], v[36:37], off
	global_load_dwordx4 v[32:35], v[36:37], off offset:1024
	v_mov_b32_e32 v45, v42
	global_load_dwordx4 v[36:39], v[40:41], off
	v_lshl_add_u64 v[54:55], v[44:45], 0, v[0:1]
	global_load_dwordx4 v[40:43], v[40:41], off offset:1024
	s_nop 0
	global_load_dwordx4 v[44:47], v[54:55], off
	global_load_dwordx4 v[48:51], v[54:55], off offset:1024
	v_mov_b32_e32 v60, 0x260
	v_lshlrev_b64 v[2:3], 10, v[2:3]
	s_waitcnt vmcnt(10)
	v_pk_add_f32 v[54:55], v[8:9], v[4:5]
	v_pk_add_f32 v[56:57], v[10:11], v[6:7]
	global_load_dwordx4 v[4:7], v0, s[8:9]
	global_load_dwordx4 v[8:11], v0, s[8:9] offset:1024
	s_waitcnt vmcnt(10)
	v_pk_add_f32 v[16:17], v[12:13], v[16:17]
	v_lshl_add_u64 v[12:13], s[4:5], 0, v[52:53]
	v_pk_add_f32 v[18:19], v[14:15], v[18:19]
	v_lshl_add_u64 v[52:53], v[12:13], 0, v[0:1]
	global_load_dwordx4 v[12:15], v0, s[10:11]
	s_mov_b32 s9, 0xf800000
	s_mov_b32 s8, 0x43000000
	s_waitcnt vmcnt(10)
	v_pk_add_f32 v[20:21], v[54:55], v[20:21]
	v_pk_add_f32 v[22:23], v[56:57], v[22:23]
	s_waitcnt vmcnt(9)
	v_pk_add_f32 v[24:25], v[16:17], v[24:25]
	v_pk_add_f32 v[26:27], v[18:19], v[26:27]
	global_load_dwordx4 v[16:19], v0, s[10:11] offset:1024
	s_waitcnt vmcnt(9)
	v_pk_add_f32 v[20:21], v[20:21], v[28:29]
	v_pk_add_f32 v[22:23], v[22:23], v[30:31]
	s_waitcnt vmcnt(8)
	v_pk_add_f32 v[24:25], v[24:25], v[32:33]
	s_waitcnt vmcnt(7)
	v_pk_add_f32 v[20:21], v[20:21], v[36:37]
	v_pk_add_f32 v[22:23], v[22:23], v[38:39]
	s_waitcnt vmcnt(5)
	v_pk_add_f32 v[20:21], v[20:21], v[44:45]
	v_pk_add_f32 v[22:23], v[22:23], v[46:47]
	v_add_f32_e32 v0, 0, v20
	v_add_f32_e32 v0, v0, v21
	v_pk_add_f32 v[24:25], v[24:25], v[40:41]
	v_add_f32_e32 v0, v0, v22
	v_pk_add_f32 v[26:27], v[26:27], v[34:35]
	s_waitcnt vmcnt(4)
	v_pk_add_f32 v[24:25], v[24:25], v[48:49]
	v_add_f32_e32 v0, v0, v23
	v_pk_add_f32 v[26:27], v[26:27], v[42:43]
	v_add_f32_e32 v0, v0, v24
	v_pk_add_f32 v[26:27], v[26:27], v[50:51]
	v_add_f32_e32 v0, v0, v25
	v_add_f32_e32 v0, v0, v26
	v_add_f32_e32 v0, v0, v27
	s_nop 1
	v_add_f32_dpp v0, v0, v0 quad_perm:[1,0,3,2] row_mask:0xf bank_mask:0xf bound_ctrl:1
	s_nop 1
	v_add_f32_dpp v0, v0, v0 quad_perm:[2,3,0,1] row_mask:0xf bank_mask:0xf bound_ctrl:1
	s_nop 1
	v_add_f32_dpp v0, v0, v0 row_half_mirror row_mask:0xf bank_mask:0xf bound_ctrl:1
	s_nop 1
	v_add_f32_dpp v0, v0, v0 row_mirror row_mask:0xf bank_mask:0xf bound_ctrl:1
	s_nop 0
	v_readlane_b32 s4, v0, 16
	v_readlane_b32 s5, v0, 48
	v_readlane_b32 s0, v0, 0
	v_readlane_b32 s1, v0, 32
	v_mov_b32_e32 v28, s4
	v_mov_b32_e32 v29, s5
	v_pk_add_f32 v[28:29], s[0:1], v[28:29]
	s_nop 0
	v_add_f32_e32 v0, v28, v29
	v_mul_f32_e32 v0, 0x3b000000, v0
	v_pk_add_f32 v[20:21], v[20:21], v[0:1] op_sel_hi:[1,0] neg_lo:[0,1] neg_hi:[0,1]
	v_pk_add_f32 v[22:23], v[22:23], v[0:1] op_sel_hi:[1,0] neg_lo:[0,1] neg_hi:[0,1]
	v_pk_mul_f32 v[28:29], v[20:21], v[20:21]
	v_pk_add_f32 v[24:25], v[24:25], v[0:1] op_sel_hi:[1,0] neg_lo:[0,1] neg_hi:[0,1]
	v_pk_add_f32 v[26:27], v[26:27], v[0:1] op_sel_hi:[1,0] neg_lo:[0,1] neg_hi:[0,1]
	v_pk_mul_f32 v[30:31], v[22:23], v[22:23]
	v_add_f32_e32 v0, v28, v29
	v_add_f32_e32 v0, v0, v30
	v_pk_mul_f32 v[32:33], v[24:25], v[24:25]
	v_add_f32_e32 v0, v0, v31
	v_add_f32_e32 v0, v0, v32
	v_pk_mul_f32 v[34:35], v[26:27], v[26:27]
	v_add_f32_e32 v0, v0, v33
	v_add_f32_e32 v0, v0, v34
	v_add_f32_e32 v0, v0, v35
	s_waitcnt vmcnt(3)
	v_pk_mul_f32 v[4:5], v[4:5], v[20:21]
	v_add_f32_dpp v0, v0, v0 quad_perm:[1,0,3,2] row_mask:0xf bank_mask:0xf bound_ctrl:1
	v_pk_mul_f32 v[6:7], v[6:7], v[22:23]
	s_waitcnt vmcnt(2)
	v_pk_mul_f32 v[8:9], v[8:9], v[24:25]
	v_add_f32_dpp v0, v0, v0 quad_perm:[2,3,0,1] row_mask:0xf bank_mask:0xf bound_ctrl:1
	v_pk_mul_f32 v[10:11], v[10:11], v[26:27]
	s_nop 0
	v_add_f32_dpp v0, v0, v0 row_half_mirror row_mask:0xf bank_mask:0xf bound_ctrl:1
	s_nop 1
	v_add_f32_dpp v0, v0, v0 row_mirror row_mask:0xf bank_mask:0xf bound_ctrl:1
	s_nop 0
	v_readlane_b32 s4, v0, 16
	v_readlane_b32 s5, v0, 48
	v_readlane_b32 s0, v0, 0
	v_readlane_b32 s1, v0, 32
	v_mov_b32_e32 v28, s4
	v_mov_b32_e32 v29, s5
	v_pk_add_f32 v[28:29], s[0:1], v[28:29]
	s_nop 0
	v_add_f32_e32 v0, v28, v29
	v_fmac_f32_e32 v59, 0x3b000000, v0
	v_mul_f32_e32 v0, 0x4f800000, v59
	v_cmp_gt_f32_e32 vcc, s9, v59
	s_nop 1
	v_cndmask_b32_e32 v0, v59, v0, vcc
	v_sqrt_f32_e32 v28, v0
	s_nop 0
	v_add_u32_e32 v20, -1, v28
	v_add_u32_e32 v21, 1, v28
	v_fma_f32 v22, -v20, v28, v0
	v_fma_f32 v23, -v21, v28, v0
	v_cmp_ge_f32_e64 s[0:1], 0, v22
	s_nop 1
	v_cndmask_b32_e64 v20, v28, v20, s[0:1]
	v_cmp_lt_f32_e64 s[0:1], 0, v23
	s_nop 1
	v_cndmask_b32_e64 v20, v20, v21, s[0:1]
	v_mul_f32_e32 v21, 0x37800000, v20
	v_cndmask_b32_e32 v20, v20, v21, vcc
	v_cmp_class_f32_e32 vcc, v0, v60
	s_nop 1
	v_cndmask_b32_e32 v0, v20, v0, vcc
	v_div_scale_f32 v20, s[0:1], v0, v0, 1.0
	v_rcp_f32_e32 v21, v20
	v_div_scale_f32 v22, vcc, 1.0, v0, 1.0
	v_fma_f32 v23, -v20, v21, 1.0
	v_fmac_f32_e32 v21, v23, v21
	v_mul_f32_e32 v23, v22, v21
	v_fma_f32 v24, -v20, v23, v22
	v_fmac_f32_e32 v23, v24, v21
	v_fma_f32 v20, -v20, v23, v22
	v_div_fmas_f32 v20, v20, v21, v23
	v_div_fixup_f32 v0, v20, v0, 1.0
	s_waitcnt vmcnt(1)
	v_pk_fma_f32 v[4:5], v[0:1], v[4:5], v[12:13] op_sel_hi:[0,1,1]
	v_pk_fma_f32 v[6:7], v[0:1], v[6:7], v[14:15] op_sel_hi:[0,1,1]
	s_waitcnt vmcnt(0)
	v_pk_fma_f32 v[8:9], v[0:1], v[8:9], v[16:17] op_sel_hi:[0,1,1]
	v_fma_mixlo_f16 v12, v4, s8, 0
	v_pk_fma_f32 v[10:11], v[0:1], v[10:11], v[18:19] op_sel_hi:[0,1,1]
	global_store_dwordx4 v[52:53], v[4:7], off sc1
	global_store_dwordx4 v[52:53], v[8:11], off offset:1024 sc1
	v_mul_f32_e32 v0, 0x43000000, v4
	v_fma_mixlo_f16 v4, v4, s8, -v12 op_sel_hi:[0,0,1]
	v_fma_mixlo_f16 v12, v8, s8, 0
	v_mul_f32_e32 v13, 0x43000000, v8
	v_fma_mixlo_f16 v8, v8, s8, -v12 op_sel_hi:[0,0,1]
	v_mul_f32_e32 v12, 0x43000000, v5
	v_fma_mixlo_f16 v14, v5, s8, 0
	v_cvt_pk_f16_f32 v12, v0, v12
	v_mul_f32_e32 v0, 0x43000000, v9
	v_pk_mul_f32 v[16:17], v[6:7], s[8:9] op_sel_hi:[1,0]
	v_fma_mixhi_f16 v4, v5, s8, -v14 op_sel_hi:[0,0,1]
	v_cvt_pk_f16_f32 v14, v13, v0
	v_cvt_pk_f16_f32 v13, v16, v17
	v_pk_mul_f32 v[18:19], v[10:11], s[8:9] op_sel_hi:[1,0]
	v_cvt_f32_f16_e32 v16, v13
	v_cvt_f32_f16_sdwa v17, v13 dst_sel:DWORD dst_unused:UNUSED_PAD src0_sel:WORD_1
	v_cvt_pk_f16_f32 v15, v18, v19
	v_cvt_f32_f16_e32 v18, v15
	v_cvt_f32_f16_sdwa v19, v15 dst_sel:DWORD dst_unused:UNUSED_PAD src0_sel:WORD_1
	v_fma_mixlo_f16 v5, v9, s8, 0
	v_pk_fma_f32 v[6:7], v[6:7], s[8:9], v[16:17] op_sel_hi:[1,0,1] neg_lo:[0,0,1] neg_hi:[0,0,1]
	v_fma_mixhi_f16 v8, v9, s8, -v5 op_sel_hi:[0,0,1]
	v_cvt_pk_f16_f32 v5, v6, v7
	v_pk_fma_f32 v[6:7], v[10:11], s[8:9], v[18:19] op_sel_hi:[1,0,1] neg_lo:[0,0,1] neg_hi:[0,0,1]
	v_lshlrev_b32_e32 v0, 1, v58
	v_cvt_pk_f16_f32 v9, v6, v7
	v_lshl_add_u64 v[6:7], s[6:7], 0, v[2:3]
	v_lshl_add_u64 v[2:3], s[2:3], 0, v[2:3]
	v_lshl_add_u64 v[6:7], v[6:7], 0, v[0:1]
	v_lshl_add_u64 v[0:1], v[2:3], 0, v[0:1]
	v_mbcnt_lo_u32_b32 v20, -1, 0
	v_mbcnt_hi_u32_b32 v20, -1, v20
	v_and_b32_e32 v20, 1, v20
	v_cmp_eq_u32_e32 vcc, 1, v20
	v_mul_u32_u24_e32 v22, 0x1f8, v20
	v_mov_b32_e32 v23, 0
	s_nop 1
	v_mov_b32_dpp v24, v12 quad_perm:[1,0,3,2] row_mask:0xf bank_mask:0xf
	v_mov_b32_dpp v25, v13 quad_perm:[1,0,3,2] row_mask:0xf bank_mask:0xf
	v_mov_b32_dpp v26, v14 quad_perm:[1,0,3,2] row_mask:0xf bank_mask:0xf
	v_mov_b32_dpp v27, v15 quad_perm:[1,0,3,2] row_mask:0xf bank_mask:0xf
	s_nop 1
	v_cndmask_b32_e32 v28, v12, v26, vcc
	v_cndmask_b32_e32 v29, v13, v27, vcc
	v_cndmask_b32_e32 v30, v24, v14, vcc
	v_cndmask_b32_e32 v31, v25, v15, vcc
	v_lshl_add_u64 v[32:33], v[6:7], 0, v[22:23]
	global_store_dwordx4 v[32:33], v[28:31], off sc1
	s_nop 1
	v_mov_b32_dpp v24, v4 quad_perm:[1,0,3,2] row_mask:0xf bank_mask:0xf
	v_mov_b32_dpp v25, v5 quad_perm:[1,0,3,2] row_mask:0xf bank_mask:0xf
	v_mov_b32_dpp v26, v8 quad_perm:[1,0,3,2] row_mask:0xf bank_mask:0xf
	v_mov_b32_dpp v27, v9 quad_perm:[1,0,3,2] row_mask:0xf bank_mask:0xf
	s_nop 1
	v_cndmask_b32_e32 v28, v4, v26, vcc
	v_cndmask_b32_e32 v29, v5, v27, vcc
	v_cndmask_b32_e32 v30, v24, v8, vcc
	v_cndmask_b32_e32 v31, v25, v9, vcc
	v_lshl_add_u64 v[32:33], v[0:1], 0, v[22:23]
	global_store_dwordx4 v[32:33], v[28:31], off sc1
	s_nop 1
	s_endpgm
	s_endpgm
	s_endpgm
	s_endpgm
	s_endpgm
	s_endpgm
	s_endpgm
	s_endpgm
	s_endpgm
	s_endpgm
	s_endpgm
	s_endpgm
	s_endpgm
	s_endpgm
	s_endpgm
	s_endpgm
	s_endpgm
	s_endpgm
	s_endpgm
	s_endpgm
	s_endpgm
	s_endpgm
	s_endpgm
	s_endpgm
	s_endpgm
	s_endpgm
	s_endpgm
	s_endpgm
	s_endpgm
	s_endpgm
	s_endpgm
	s_endpgm
	s_endpgm
	s_endpgm
	s_endpgm
	s_endpgm
	s_endpgm
	s_endpgm
	s_endpgm

.LBB22_5:
	v_lshlrev_b32_e32 v0, 2, v0
	v_and_b32_e32 v66, 0xfc, v0
	v_lshlrev_b64 v[4:5], 11, v[4:5]
	v_lshlrev_b32_e32 v0, 2, v66
	v_mov_b32_e32 v1, 0
	s_waitcnt lgkmcnt(0)
	v_lshl_add_u64 v[4:5], s[18:19], 0, v[4:5]
	v_lshl_add_u64 v[20:21], v[4:5], 0, v[0:1]
	global_load_dwordx4 v[4:7], v[20:21], off
	global_load_dwordx4 v[8:11], v0, s[16:17]
	global_load_dwordx4 v[12:15], v0, s[16:17] offset:1024
	global_load_dwordx4 v[16:19], v[20:21], off offset:1024
	v_lshlrev_b64 v[48:49], 11, v[2:3]
	v_lshl_add_u64 v[40:41], s[14:15], 0, v[48:49]
	v_lshl_add_u64 v[28:29], v[40:41], 0, v[0:1]
	global_load_dwordx4 v[20:23], v[28:29], off
	global_load_dwordx4 v[24:27], v[28:29], off offset:1024
	v_lshlrev_b64 v[2:3], 10, v[2:3]
	s_waitcnt lgkmcnt(0)
	v_lshl_add_u64 v[28:29], s[0:1], 2, v[40:41]
	v_lshl_add_u64 v[42:43], v[28:29], 0, v[0:1]
	v_mad_u64_u32 v[36:37], s[12:13], s0, 12, v[40:41]
	v_lshl_add_u64 v[32:33], s[0:1], 3, v[40:41]
	global_load_dwordx4 v[28:31], v[42:43], off
	v_mov_b32_e32 v38, v37
	v_lshl_add_u64 v[44:45], v[32:33], 0, v[0:1]
	v_mad_u64_u32 v[38:39], s[12:13], s1, 12, v[38:39]
	global_load_dwordx4 v[32:35], v[44:45], off
	v_mov_b32_e32 v37, v38
	v_lshl_add_u64 v[46:47], v[36:37], 0, v[0:1]
	global_load_dwordx4 v[36:39], v[46:47], off
	v_mad_u64_u32 v[52:53], s[12:13], s0, 20, v[40:41]
	v_mad_u64_u32 v[54:55], s[12:13], s0, 24, v[40:41]
	v_lshl_add_u64 v[50:51], s[0:1], 4, v[40:41]
	v_mad_u64_u32 v[40:41], s[12:13], s0, 28, v[40:41]
	v_lshl_add_u64 v[50:51], v[50:51], 0, v[0:1]
	s_waitcnt vmcnt(7)
	v_pk_add_f32 v[56:57], v[8:9], v[4:5]
	v_mov_b32_e32 v4, v53
	v_pk_add_f32 v[58:59], v[10:11], v[6:7]
	v_mov_b32_e32 v6, v55
	v_mad_u64_u32 v[10:11], s[12:13], s1, 20, v[4:5]
	s_waitcnt vmcnt(5)
	v_pk_add_f32 v[60:61], v[12:13], v[16:17]
	v_mov_b32_e32 v8, v41
	v_mad_u64_u32 v[12:13], s[12:13], s1, 24, v[6:7]
	v_mov_b32_e32 v53, v10
	v_pk_add_f32 v[62:63], v[14:15], v[18:19]
	v_mad_u64_u32 v[14:15], s[0:1], s1, 28, v[8:9]
	global_load_dwordx4 v[4:7], v[50:51], off
	v_mov_b32_e32 v55, v12
	v_lshl_add_u64 v[52:53], v[52:53], 0, v[0:1]
	v_mov_b32_e32 v41, v14
	v_lshl_add_u64 v[54:55], v[54:55], 0, v[0:1]
	global_load_dwordx4 v[12:15], v[52:53], off
	v_lshl_add_u64 v[64:65], v[40:41], 0, v[0:1]
	global_load_dwordx4 v[16:19], v[54:55], off
	global_load_dwordx4 v[8:11], v[42:43], off offset:1024
	s_waitcnt vmcnt(8)
	v_pk_add_f32 v[40:41], v[56:57], v[20:21]
	v_pk_add_f32 v[42:43], v[58:59], v[22:23]
	global_load_dwordx4 v[20:23], v[64:65], off
	s_waitcnt vmcnt(8)
	v_pk_add_f32 v[56:57], v[60:61], v[24:25]
	v_pk_add_f32 v[58:59], v[62:63], v[26:27]
	s_waitcnt vmcnt(7)
	v_pk_add_f32 v[40:41], v[40:41], v[28:29]
	v_pk_add_f32 v[42:43], v[42:43], v[30:31]
	global_load_dwordx4 v[24:27], v[44:45], off offset:1024
	global_load_dwordx4 v[28:31], v[46:47], off offset:1024
	s_waitcnt vmcnt(8)
	v_pk_add_f32 v[44:45], v[40:41], v[32:33]
	v_pk_add_f32 v[46:47], v[42:43], v[34:35]
	global_load_dwordx4 v[32:35], v[50:51], off offset:1024
	global_load_dwordx4 v[40:43], v[52:53], off offset:1024
	s_waitcnt vmcnt(9)
	v_pk_add_f32 v[50:51], v[44:45], v[36:37]
	v_pk_add_f32 v[52:53], v[46:47], v[38:39]
	global_load_dwordx4 v[36:39], v[54:55], off offset:1024
	global_load_dwordx4 v[44:47], v[64:65], off offset:1024
	s_waitcnt vmcnt(10)
	v_pk_add_f32 v[4:5], v[50:51], v[4:5]
	v_pk_add_f32 v[6:7], v[52:53], v[6:7]
	s_waitcnt vmcnt(9)
	v_pk_add_f32 v[50:51], v[4:5], v[12:13]
	v_pk_add_f32 v[52:53], v[6:7], v[14:15]
	global_load_dwordx4 v[4:7], v0, s[8:9]
	global_load_dwordx4 v[12:15], v0, s[10:11]
	s_waitcnt vmcnt(10)
	v_pk_add_f32 v[16:17], v[50:51], v[16:17]
	v_pk_add_f32 v[18:19], v[52:53], v[18:19]
	s_waitcnt vmcnt(9)
	v_pk_add_f32 v[8:9], v[56:57], v[8:9]
	s_waitcnt vmcnt(8)
	v_pk_add_f32 v[50:51], v[16:17], v[20:21]
	v_pk_add_f32 v[52:53], v[18:19], v[22:23]
	global_load_dwordx4 v[16:19], v0, s[8:9] offset:1024
	global_load_dwordx4 v[20:23], v0, s[10:11] offset:1024
	v_pk_add_f32 v[10:11], v[58:59], v[10:11]
	s_waitcnt vmcnt(9)
	v_pk_add_f32 v[8:9], v[8:9], v[24:25]
	v_add_f32_e32 v24, 0, v50
	s_waitcnt vmcnt(8)
	v_pk_add_f32 v[8:9], v[8:9], v[28:29]
	v_pk_add_f32 v[10:11], v[10:11], v[26:27]
	s_waitcnt vmcnt(7)
	v_pk_add_f32 v[8:9], v[8:9], v[32:33]
	v_add_f32_e32 v24, v24, v51
	s_waitcnt vmcnt(6)
	v_pk_add_f32 v[8:9], v[8:9], v[40:41]
	v_pk_add_f32 v[10:11], v[10:11], v[30:31]
	v_add_f32_e32 v24, v24, v52
	s_waitcnt vmcnt(5)
	v_pk_add_f32 v[8:9], v[8:9], v[36:37]
	v_pk_add_f32 v[10:11], v[10:11], v[34:35]
	v_add_f32_e32 v24, v24, v53
	s_waitcnt vmcnt(4)
	v_pk_add_f32 v[8:9], v[8:9], v[44:45]
	v_pk_add_f32 v[10:11], v[10:11], v[42:43]
	v_add_f32_e32 v24, v24, v8
	v_pk_add_f32 v[10:11], v[10:11], v[38:39]
	v_add_f32_e32 v24, v24, v9
	v_pk_add_f32 v[10:11], v[10:11], v[46:47]
	s_nop 0
	v_add_f32_e32 v24, v24, v10
	v_add_f32_e32 v24, v24, v11
	s_nop 1
	v_add_f32_dpp v24, v24, v24 quad_perm:[1,0,3,2] row_mask:0xf bank_mask:0xf bound_ctrl:1
	s_nop 1
	v_add_f32_dpp v24, v24, v24 quad_perm:[2,3,0,1] row_mask:0xf bank_mask:0xf bound_ctrl:1
	s_nop 1
	v_add_f32_dpp v24, v24, v24 row_half_mirror row_mask:0xf bank_mask:0xf bound_ctrl:1
	s_nop 1
	v_add_f32_dpp v24, v24, v24 row_mirror row_mask:0xf bank_mask:0xf bound_ctrl:1
	s_nop 0
	v_readlane_b32 s8, v24, 16
	v_readlane_b32 s9, v24, 48
	v_readlane_b32 s0, v24, 0
	v_readlane_b32 s1, v24, 32
	v_mov_b32_e32 v24, s8
	v_mov_b32_e32 v25, s9
	v_pk_add_f32 v[24:25], s[0:1], v[24:25]
	s_nop 0
	v_add_f32_e32 v24, v24, v25
	v_mul_f32_e32 v24, 0x3b000000, v24
	v_pk_add_f32 v[26:27], v[50:51], v[24:25] op_sel_hi:[1,0] neg_lo:[0,1] neg_hi:[0,1]
	v_pk_add_f32 v[30:31], v[52:53], v[24:25] op_sel_hi:[1,0] neg_lo:[0,1] neg_hi:[0,1]
	v_pk_mul_f32 v[28:29], v[26:27], v[26:27]
	v_pk_mul_f32 v[32:33], v[30:31], v[30:31]
	v_add_f32_e32 v28, v28, v29
	v_pk_add_f32 v[8:9], v[8:9], v[24:25] op_sel_hi:[1,0] neg_lo:[0,1] neg_hi:[0,1]
	v_add_f32_e32 v28, v28, v32
	v_pk_mul_f32 v[34:35], v[8:9], v[8:9]
	v_add_f32_e32 v28, v28, v33
	v_pk_add_f32 v[10:11], v[10:11], v[24:25] op_sel_hi:[1,0] neg_lo:[0,1] neg_hi:[0,1]
	v_add_f32_e32 v28, v28, v34
	v_pk_mul_f32 v[24:25], v[10:11], v[10:11]
	v_add_f32_e32 v28, v28, v35
	v_add_f32_e32 v24, v28, v24
	v_add_f32_e32 v24, v24, v25
	s_waitcnt vmcnt(3)
	v_pk_mul_f32 v[4:5], v[4:5], v[26:27]
	v_add_f32_dpp v24, v24, v24 quad_perm:[1,0,3,2] row_mask:0xf bank_mask:0xf bound_ctrl:1
	v_pk_mul_f32 v[6:7], v[6:7], v[30:31]
	s_waitcnt vmcnt(1)
	v_pk_mul_f32 v[8:9], v[16:17], v[8:9]
	v_add_f32_dpp v24, v24, v24 quad_perm:[2,3,0,1] row_mask:0xf bank_mask:0xf bound_ctrl:1
	v_pk_mul_f32 v[10:11], v[18:19], v[10:11]
	s_nop 0
	v_add_f32_dpp v24, v24, v24 row_half_mirror row_mask:0xf bank_mask:0xf bound_ctrl:1
	s_nop 1
	v_add_f32_dpp v24, v24, v24 row_mirror row_mask:0xf bank_mask:0xf bound_ctrl:1
	s_nop 0
	v_readlane_b32 s8, v24, 16
	v_readlane_b32 s9, v24, 48
	v_readlane_b32 s0, v24, 0
	v_readlane_b32 s1, v24, 32
	v_mov_b32_e32 v24, s8
	v_mov_b32_e32 v25, s9
	v_pk_add_f32 v[24:25], s[0:1], v[24:25]
	s_mov_b32 s0, 0xf800000
	v_add_f32_e32 v24, v24, v25
	v_mov_b32_e32 v25, 0x3727c5ac
	v_fmac_f32_e32 v25, 0x3b000000, v24
	v_mul_f32_e32 v24, 0x4f800000, v25
	v_cmp_gt_f32_e32 vcc, s0, v25
	s_nop 1
	v_cndmask_b32_e32 v24, v25, v24, vcc
	v_sqrt_f32_e32 v25, v24
	s_nop 0
	v_add_u32_e32 v28, -1, v25
	v_fma_f32 v29, -v28, v25, v24
	v_cmp_ge_f32_e64 s[0:1], 0, v29
	v_add_u32_e32 v29, 1, v25
	s_nop 0
	v_cndmask_b32_e64 v28, v25, v28, s[0:1]
	v_fma_f32 v25, -v29, v25, v24
	v_cmp_lt_f32_e64 s[0:1], 0, v25
	s_nop 1
	v_cndmask_b32_e64 v25, v28, v29, s[0:1]
	v_mul_f32_e32 v28, 0x37800000, v25
	v_cndmask_b32_e32 v25, v25, v28, vcc
	v_mov_b32_e32 v28, 0x260
	v_cmp_class_f32_e32 vcc, v24, v28
	s_nop 1
	v_cndmask_b32_e32 v28, v25, v24, vcc
	v_div_scale_f32 v29, s[0:1], v28, v28, 1.0
	v_rcp_f32_e32 v32, v29
	v_lshl_add_u64 v[24:25], s[4:5], 0, v[48:49]
	v_lshl_add_u64 v[24:25], v[24:25], 0, v[0:1]
	s_mov_b32 s0, 0x43000000
	v_fma_f32 v0, -v29, v32, 1.0
	v_fmac_f32_e32 v32, v0, v32
	v_div_scale_f32 v0, vcc, 1.0, v28, 1.0
	v_mul_f32_e32 v33, v0, v32
	v_fma_f32 v34, -v29, v33, v0
	v_fmac_f32_e32 v33, v34, v32
	v_fma_f32 v0, -v29, v33, v0
	v_div_fmas_f32 v0, v0, v32, v33
	v_div_fixup_f32 v0, v0, v28, 1.0
	v_pk_fma_f32 v[4:5], v[0:1], v[4:5], v[12:13] op_sel_hi:[0,1,1]
	v_pk_fma_f32 v[6:7], v[0:1], v[6:7], v[14:15] op_sel_hi:[0,1,1]
	s_waitcnt vmcnt(0)
	v_pk_fma_f32 v[8:9], v[0:1], v[8:9], v[20:21] op_sel_hi:[0,1,1]
	v_fma_mixlo_f16 v12, v4, s0, 0
	v_pk_fma_f32 v[10:11], v[0:1], v[10:11], v[22:23] op_sel_hi:[0,1,1]
	global_store_dwordx4 v[24:25], v[4:7], off sc1
	global_store_dwordx4 v[24:25], v[8:11], off offset:1024 sc1
	v_mul_f32_e32 v0, 0x43000000, v4
	v_fma_mixlo_f16 v4, v4, s0, -v12 op_sel_hi:[0,0,1]
	v_fma_mixlo_f16 v12, v8, s0, 0
	v_mul_f32_e32 v13, 0x43000000, v8
	v_fma_mixlo_f16 v8, v8, s0, -v12 op_sel_hi:[0,0,1]
	v_mul_f32_e32 v12, 0x43000000, v5
	v_fma_mixlo_f16 v14, v5, s0, 0
	v_cvt_pk_f16_f32 v12, v0, v12
	v_mul_f32_e32 v0, 0x43000000, v9
	v_pk_mul_f32 v[16:17], v[6:7], s[0:1] op_sel_hi:[1,0]
	v_fma_mixhi_f16 v4, v5, s0, -v14 op_sel_hi:[0,0,1]
	v_cvt_pk_f16_f32 v14, v13, v0
	v_cvt_pk_f16_f32 v13, v16, v17
	v_pk_mul_f32 v[18:19], v[10:11], s[0:1] op_sel_hi:[1,0]
	v_cvt_f32_f16_e32 v16, v13
	v_cvt_f32_f16_sdwa v17, v13 dst_sel:DWORD dst_unused:UNUSED_PAD src0_sel:WORD_1
	v_cvt_pk_f16_f32 v15, v18, v19
	v_cvt_f32_f16_e32 v18, v15
	v_cvt_f32_f16_sdwa v19, v15 dst_sel:DWORD dst_unused:UNUSED_PAD src0_sel:WORD_1
	v_fma_mixlo_f16 v5, v9, s0, 0
	v_pk_fma_f32 v[6:7], v[6:7], s[0:1], v[16:17] op_sel_hi:[1,0,1] neg_lo:[0,0,1] neg_hi:[0,0,1]
	v_fma_mixhi_f16 v8, v9, s0, -v5 op_sel_hi:[0,0,1]
	v_cvt_pk_f16_f32 v5, v6, v7
	v_pk_fma_f32 v[6:7], v[10:11], s[0:1], v[18:19] op_sel_hi:[1,0,1] neg_lo:[0,0,1] neg_hi:[0,0,1]
	v_lshlrev_b32_e32 v0, 1, v66
	v_cvt_pk_f16_f32 v9, v6, v7
	v_lshl_add_u64 v[6:7], s[6:7], 0, v[2:3]
	v_lshl_add_u64 v[2:3], s[2:3], 0, v[2:3]
	v_lshl_add_u64 v[6:7], v[6:7], 0, v[0:1]
	v_lshl_add_u64 v[0:1], v[2:3], 0, v[0:1]
	v_mbcnt_lo_u32_b32 v20, -1, 0
	v_mbcnt_hi_u32_b32 v20, -1, v20
	v_and_b32_e32 v20, 1, v20
	v_cmp_eq_u32_e32 vcc, 1, v20
	v_mul_u32_u24_e32 v22, 0x1f8, v20
	v_mov_b32_e32 v23, 0
	s_nop 1
	v_mov_b32_dpp v24, v12 quad_perm:[1,0,3,2] row_mask:0xf bank_mask:0xf
	v_mov_b32_dpp v25, v13 quad_perm:[1,0,3,2] row_mask:0xf bank_mask:0xf
	v_mov_b32_dpp v26, v14 quad_perm:[1,0,3,2] row_mask:0xf bank_mask:0xf
	v_mov_b32_dpp v27, v15 quad_perm:[1,0,3,2] row_mask:0xf bank_mask:0xf
	s_nop 1
	v_cndmask_b32_e32 v28, v12, v26, vcc
	v_cndmask_b32_e32 v29, v13, v27, vcc
	v_cndmask_b32_e32 v30, v24, v14, vcc
	v_cndmask_b32_e32 v31, v25, v15, vcc
	v_lshl_add_u64 v[32:33], v[6:7], 0, v[22:23]
	global_store_dwordx4 v[32:33], v[28:31], off sc1
	s_nop 1
	v_mov_b32_dpp v24, v4 quad_perm:[1,0,3,2] row_mask:0xf bank_mask:0xf
	v_mov_b32_dpp v25, v5 quad_perm:[1,0,3,2] row_mask:0xf bank_mask:0xf
	v_mov_b32_dpp v26, v8 quad_perm:[1,0,3,2] row_mask:0xf bank_mask:0xf
	v_mov_b32_dpp v27, v9 quad_perm:[1,0,3,2] row_mask:0xf bank_mask:0xf
	s_nop 1
	v_cndmask_b32_e32 v28, v4, v26, vcc
	v_cndmask_b32_e32 v29, v5, v27, vcc
	v_cndmask_b32_e32 v30, v24, v8, vcc
	v_cndmask_b32_e32 v31, v25, v9, vcc
	v_lshl_add_u64 v[32:33], v[0:1], 0, v[22:23]
	global_store_dwordx4 v[32:33], v[28:31], off sc1
	s_nop 1
	s_endpgm
	s_endpgm
	s_endpgm
	s_endpgm
	s_endpgm
	s_endpgm
	s_endpgm
	s_endpgm
	s_endpgm
	s_endpgm
	s_endpgm
	s_endpgm
	s_endpgm
	s_endpgm
	s_endpgm
	s_endpgm
	s_endpgm
	s_endpgm
	s_endpgm
	s_endpgm
